# v33 + LayerNorm / final-combine wave reductions (sum, variance, absmax) via DPP and permlane swaps instead of six ds_bpermute round trips each (bit-identical)
# speedup vs baseline: 1.0015x; 1.0015x over previous
.LBB0_416:
	s_waitcnt vmcnt(23)
	v_mov_b64_e32 v[50:51], v[34:35]
	s_waitcnt vmcnt(22)
	v_mov_b64_e32 v[56:57], v[36:37]
	v_lshlrev_b32_e32 v59, 16, v50
	v_lshlrev_b32_e32 v58, 16, v56
	v_and_b32_e32 v61, 0xffff0000, v50
	v_and_b32_e32 v60, 0xffff0000, v56
	v_lshlrev_b32_e32 v53, 16, v51
	v_lshlrev_b32_e32 v52, 16, v57
	v_and_b32_e32 v55, 0xffff0000, v51
	v_and_b32_e32 v54, 0xffff0000, v57
	v_pk_add_f32 v[50:51], v[58:59], v[60:61]
	v_pk_add_f32 v[56:57], v[52:53], v[54:55]
	s_waitcnt vmcnt(21)
	v_mov_b64_e32 v[62:63], v[38:39]
	v_pk_add_f32 v[50:51], v[50:51], v[56:57]
	s_waitcnt vmcnt(20)
	v_lshlrev_b32_e32 v44, 16, v27
	v_and_b32_e32 v45, 0xffff0000, v27
	v_add_f32_e32 v27, 0, v51
	v_add_f32_e32 v47, v50, v27
	v_lshlrev_b32_e32 v51, 16, v63
	v_lshlrev_b32_e32 v50, 16, v62
	v_and_b32_e32 v77, 0xffff0000, v63
	v_and_b32_e32 v76, 0xffff0000, v62
	v_pk_add_f32 v[56:57], v[50:51], v[76:77]
	v_lshlrev_b32_e32 v42, 16, v26
	v_and_b32_e32 v43, 0xffff0000, v26
	v_pk_add_f32 v[56:57], v[56:57], v[56:57] op_sel_hi:[0,1]
	s_waitcnt vmcnt(18)
	v_mov_b64_e32 v[64:65], v[40:41]
	v_lshlrev_b32_e32 v40, 16, v32
	v_and_b32_e32 v48, 0xffff0000, v32
	v_lshlrev_b32_e32 v38, 16, v33
	v_and_b32_e32 v46, 0xffff0000, v33
	v_add_f32_e32 v41, v42, v43
	v_add_f32_e32 v49, v44, v45
	v_mov_b32_e32 v39, v57
	v_pk_add_f32 v[62:63], v[40:41], v[48:49]
	v_pk_add_f32 v[56:57], v[38:39], v[46:47]
	v_and_b32_e32 v79, 0xffff0000, v65
	v_pk_add_f32 v[56:57], v[62:63], v[56:57]
	v_and_b32_e32 v78, 0xffff0000, v64
	v_pk_add_f32 v[62:63], v[56:57], v[56:57] op_sel_hi:[0,1]
	v_lshlrev_b32_e32 v57, 16, v65
	v_lshlrev_b32_e32 v56, 16, v64
	v_pk_add_f32 v[64:65], v[56:57], v[78:79]
	s_waitcnt vmcnt(17)
	v_lshlrev_b32_e32 v32, 16, v28
	v_and_b32_e32 v33, 0xffff0000, v28
	v_lshlrev_b32_e32 v36, 16, v29
	v_and_b32_e32 v37, 0xffff0000, v29
	v_pk_add_f32 v[64:65], v[64:65], v[64:65] op_sel_hi:[0,1]
	s_waitcnt vmcnt(16)
	v_lshlrev_b32_e32 v28, 16, v30
	v_and_b32_e32 v34, 0xffff0000, v30
	v_lshlrev_b32_e32 v26, 16, v31
	v_and_b32_e32 v30, 0xffff0000, v31
	v_add_f32_e32 v29, v32, v33
	v_add_f32_e32 v35, v36, v37
	v_mov_b32_e32 v27, v65
	v_mov_b32_e32 v31, v63
	v_pk_add_f32 v[80:81], v[28:29], v[34:35]
	v_pk_add_f32 v[62:63], v[26:27], v[30:31]
	s_nop 0
	v_pk_add_f32 v[62:63], v[80:81], v[62:63]
	s_nop 0
	v_add_f32_e32 v27, v62, v63
	s_nop 1
	v_mov_b32_dpp v29, v27 quad_perm:[1,0,3,2] row_mask:0xf bank_mask:0xf
	s_waitcnt lgkmcnt(0)
	v_add_f32_e32 v27, v27, v29
	s_nop 1
	v_mov_b32_dpp v29, v27 quad_perm:[2,3,0,1] row_mask:0xf bank_mask:0xf
	s_waitcnt lgkmcnt(0)
	v_add_f32_e32 v27, v27, v29
	s_nop 1
	v_mov_b32_dpp v29, v27 row_half_mirror row_mask:0xf bank_mask:0xf
	s_waitcnt lgkmcnt(0)
	v_add_f32_e32 v27, v27, v29
	s_nop 1
	v_mov_b32_dpp v29, v27 row_mirror row_mask:0xf bank_mask:0xf
	s_waitcnt lgkmcnt(0)
	v_add_f32_e32 v27, v27, v29
	v_mov_b32_e32 v29, v27
	s_nop 1
	v_permlane16_swap_b32_e32 v29, v27
	s_waitcnt lgkmcnt(0)
	v_add_f32_e32 v27, v27, v29
	v_mov_b32_e32 v29, v27
	s_nop 1
	v_permlane32_swap_b32_e32 v29, v27
	s_waitcnt lgkmcnt(0)
	v_add_f32_e32 v27, v27, v29
	v_fmac_f32_e32 v61, 0xba000000, v27
	v_fmac_f32_e32 v60, 0xba000000, v27
	v_fmac_f32_e32 v55, 0xba000000, v27
	v_fmac_f32_e32 v59, 0xba000000, v27
	v_fmac_f32_e32 v54, 0xba000000, v27
	v_fmac_f32_e32 v58, 0xba000000, v27
	v_mov_b32_e32 v64, v61
	v_mov_b32_e32 v65, v60
	v_fmac_f32_e32 v53, 0xba000000, v27
	v_fmac_f32_e32 v52, 0xba000000, v27
	v_mov_b32_e32 v62, v59
	v_mov_b32_e32 v63, v58
	v_pk_mul_f32 v[64:65], v[64:65], v[64:65]
	v_mov_b32_e32 v80, v55
	v_mov_b32_e32 v81, v54
	v_pk_fma_f32 v[62:63], v[62:63], v[62:63], v[64:65]
	v_mov_b32_e32 v64, v53
	v_mov_b32_e32 v65, v52
	v_pk_mul_f32 v[80:81], v[80:81], v[80:81]
	v_fmac_f32_e32 v76, 0xba000000, v27
	v_pk_fma_f32 v[64:65], v[64:65], v[64:65], v[80:81]
	v_fmac_f32_e32 v77, 0xba000000, v27
	v_pk_add_f32 v[62:63], v[62:63], v[64:65]
	v_fmac_f32_e32 v51, 0xba000000, v27
	v_pk_add_f32 v[64:65], v[62:63], v[62:63] op_sel_hi:[0,1]
	v_fmac_f32_e32 v50, 0xba000000, v27
	v_mov_b32_e32 v62, v51
	v_mov_b32_e32 v63, v77
	v_mov_b32_e32 v51, v76
	v_pk_mul_f32 v[80:81], v[62:63], v[62:63]
	v_pk_mul_f32 v[76:77], v[50:51], v[50:51]
	v_fmac_f32_e32 v42, 0xba000000, v27
	v_pk_mov_b32 v[82:83], v[76:77], v[80:81] op_sel:[1,0]
	v_mov_b32_e32 v77, v81
	v_fmac_f32_e32 v43, 0xba000000, v27
	v_fmac_f32_e32 v44, 0xba000000, v27
	v_mul_f32_e32 v64, v42, v42
	v_pk_add_f32 v[76:77], v[82:83], v[76:77]
	v_fmac_f32_e32 v45, 0xba000000, v27
	v_pk_fma_f32 v[80:81], v[42:43], v[42:43], v[64:65] op_sel_hi:[1,1,0]
	v_mul_f32_e32 v64, v44, v44
	v_pk_add_f32 v[76:77], v[76:77], v[76:77] op_sel_hi:[0,1]
	v_pk_fma_f32 v[82:83], v[44:45], v[44:45], v[64:65] op_sel_hi:[1,1,0]
	v_fmac_f32_e32 v46, 0xba000000, v27
	v_fmac_f32_e32 v38, 0xba000000, v27
	v_fmac_f32_e32 v48, 0xba000000, v27
	v_fmac_f32_e32 v40, 0xba000000, v27
	v_mul_f32_e32 v80, v40, v40
	v_mul_f32_e32 v82, v48, v48
	v_mul_f32_e32 v76, v38, v38
	v_mul_f32_e32 v64, v46, v46
	v_pk_add_f32 v[80:81], v[80:81], v[82:83]
	v_pk_add_f32 v[64:65], v[76:77], v[64:65]
	v_fmac_f32_e32 v78, 0xba000000, v27
	v_pk_add_f32 v[64:65], v[80:81], v[64:65]
	v_fmac_f32_e32 v79, 0xba000000, v27
	v_fmac_f32_e32 v57, 0xba000000, v27
	v_pk_add_f32 v[76:77], v[64:65], v[64:65] op_sel_hi:[0,1]
	v_fmac_f32_e32 v56, 0xba000000, v27
	v_mov_b32_e32 v64, v57
	v_mov_b32_e32 v65, v79
	v_mov_b32_e32 v57, v78
	v_pk_mul_f32 v[80:81], v[64:65], v[64:65]
	v_pk_mul_f32 v[78:79], v[56:57], v[56:57]
	v_fmac_f32_e32 v32, 0xba000000, v27
	v_pk_mov_b32 v[82:83], v[78:79], v[80:81] op_sel:[1,0]
	v_mov_b32_e32 v79, v81
	v_fmac_f32_e32 v33, 0xba000000, v27
	v_fmac_f32_e32 v36, 0xba000000, v27
	v_mul_f32_e32 v76, v32, v32
	v_pk_add_f32 v[78:79], v[82:83], v[78:79]
	v_fmac_f32_e32 v37, 0xba000000, v27
	v_pk_fma_f32 v[80:81], v[32:33], v[32:33], v[76:77] op_sel_hi:[1,1,0]
	v_mul_f32_e32 v76, v36, v36
	v_pk_add_f32 v[78:79], v[78:79], v[78:79] op_sel_hi:[0,1]
	v_pk_fma_f32 v[82:83], v[36:37], v[36:37], v[76:77] op_sel_hi:[1,1,0]
	v_fmac_f32_e32 v30, 0xba000000, v27
	v_fmac_f32_e32 v26, 0xba000000, v27
	v_fmac_f32_e32 v34, 0xba000000, v27
	v_fmac_f32_e32 v28, 0xba000000, v27
	v_mul_f32_e32 v80, v28, v28
	v_mul_f32_e32 v82, v34, v34
	v_mul_f32_e32 v78, v26, v26
	v_mul_f32_e32 v76, v30, v30
	v_pk_add_f32 v[80:81], v[80:81], v[82:83]
	v_pk_add_f32 v[76:77], v[78:79], v[76:77]
	v_mov_b32_e32 v140, v58
	v_pk_add_f32 v[76:77], v[80:81], v[76:77]
	v_mov_b32_e32 v141, v60
	v_add_f32_e32 v27, v76, v77
	global_load_dwordx4 v[76:79], v[2:3], off
	global_load_dwordx4 v[80:83], v[4:5], off
	global_load_dwordx4 v[84:87], v[2:3], off offset:1024
	global_load_dwordx4 v[88:91], v[4:5], off offset:1024
	global_load_dwordx4 v[92:95], v[2:3], off offset:2048
	global_load_dwordx4 v[96:99], v[4:5], off offset:2048
	global_load_dwordx4 v[100:103], v[2:3], off offset:3072
	global_load_dwordx4 v[104:107], v[4:5], off offset:3072
	global_load_dwordx4 v[108:111], v[6:7], off
	global_load_dwordx4 v[112:115], v[8:9], off
	global_load_dwordx4 v[116:119], v[10:11], off
	global_load_dwordx4 v[120:123], v[12:13], off
	global_load_dwordx4 v[124:127], v[14:15], off
	global_load_dwordx4 v[128:131], v[16:17], off
	global_load_dwordx4 v[132:135], v[18:19], off
	global_load_dwordx4 v[136:139], v[20:21], off
	s_nop 1
	v_mov_b32_dpp v29, v27 quad_perm:[1,0,3,2] row_mask:0xf bank_mask:0xf
	v_mov_b32_e32 v60, v59
	v_mov_b32_e32 v58, v52
	v_mov_b32_e32 v59, v54
	v_mov_b32_e32 v54, v53
	s_waitcnt lgkmcnt(0)
	v_add_f32_e32 v27, v27, v29
	s_nop 1
	v_mov_b32_dpp v29, v27 quad_perm:[2,3,0,1] row_mask:0xf bank_mask:0xf
	s_waitcnt lgkmcnt(0)
	v_add_f32_e32 v27, v27, v29
	s_nop 1
	v_mov_b32_dpp v29, v27 row_half_mirror row_mask:0xf bank_mask:0xf
	s_waitcnt lgkmcnt(0)
	v_add_f32_e32 v27, v27, v29
	s_nop 1
	v_mov_b32_dpp v29, v27 row_mirror row_mask:0xf bank_mask:0xf
	s_waitcnt lgkmcnt(0)
	v_add_f32_e32 v27, v27, v29
	v_mov_b32_e32 v29, v27
	s_nop 1
	v_permlane16_swap_b32_e32 v29, v27
	s_waitcnt lgkmcnt(0)
	v_add_f32_e32 v27, v27, v29
	v_mov_b32_e32 v29, v27
	s_nop 1
	v_permlane32_swap_b32_e32 v29, v27
	s_waitcnt lgkmcnt(0)
	v_add_f32_e32 v27, v27, v29
	v_fmamk_f32 v27, v27, 0x3a000000, v72
	v_mul_f32_e32 v29, 0x4f800000, v27
	v_cmp_gt_f32_e32 vcc, s7, v27
	s_nop 1
	v_cndmask_b32_e32 v27, v27, v29, vcc
	v_sqrt_f32_e32 v29, v27
	s_nop 0
	v_add_u32_e32 v31, -1, v29
	v_fma_f32 v35, -v31, v29, v27
	v_cmp_ge_f32_e64 s[2:3], 0, v35
	v_add_u32_e32 v35, 1, v29
	s_nop 0
	v_cndmask_b32_e64 v31, v29, v31, s[2:3]
	v_fma_f32 v29, -v35, v29, v27
	v_cmp_lt_f32_e64 s[2:3], 0, v29
	s_nop 1
	v_cndmask_b32_e64 v29, v31, v35, s[2:3]
	v_mul_f32_e32 v31, 0x37800000, v29
	v_cndmask_b32_e32 v29, v29, v31, vcc
	v_cmp_class_f32_e32 vcc, v27, v73
	s_nop 1
	v_cndmask_b32_e32 v27, v29, v27, vcc
	v_div_scale_f32 v29, s[2:3], v27, v27, 1.0
	v_rcp_f32_e32 v31, v29
	s_mov_b32 s2, s6
	s_add_i32 s6, s6, s8
	s_cmpk_gt_i32 s6, 0x3fff
	v_fma_f32 v35, -v29, v31, 1.0
	v_fmac_f32_e32 v31, v35, v31
	v_div_scale_f32 v35, vcc, 1.0, v27, 1.0
	v_mul_f32_e32 v39, v35, v31
	v_fma_f32 v41, -v29, v39, v35
	v_fmac_f32_e32 v39, v41, v31
	v_fma_f32 v29, -v29, v39, v35
	v_div_fmas_f32 v29, v29, v31, v39
	v_div_fixup_f32 v52, v29, v27, 1.0
	v_pk_mul_f32 v[60:61], v[60:61], v[52:53] op_sel_hi:[1,0]
	v_pk_mul_f32 v[54:55], v[54:55], v[52:53] op_sel_hi:[1,0]
	v_mov_b32_e32 v41, v48
	v_mov_b32_e32 v39, v46
	v_mov_b32_e32 v27, v30
	s_waitcnt vmcnt(14)
	v_pk_fma_f32 v[54:55], v[78:79], v[54:55], v[82:83]
	v_pk_fma_f32 v[60:61], v[76:77], v[60:61], v[80:81]
	v_pk_mul_f32 v[76:77], v[140:141], v[52:53] op_sel_hi:[1,0]
	v_pk_mul_f32 v[58:59], v[58:59], v[52:53] op_sel_hi:[1,0]
	v_pk_mul_f32 v[40:41], v[40:41], v[52:53] op_sel_hi:[1,0]
	v_pk_mul_f32 v[38:39], v[38:39], v[52:53] op_sel_hi:[1,0]
	v_mov_b32_e32 v29, v34
	v_pk_mul_f32 v[26:27], v[26:27], v[52:53] op_sel_hi:[1,0]
	s_waitcnt vmcnt(12)
	v_pk_fma_f32 v[58:59], v[86:87], v[58:59], v[90:91]
	v_pk_fma_f32 v[76:77], v[84:85], v[76:77], v[88:89]
	v_pk_mul_f32 v[50:51], v[50:51], v[52:53] op_sel_hi:[1,0]
	v_pk_mul_f32 v[62:63], v[62:63], v[52:53] op_sel_hi:[1,0]
	v_pk_mul_f32 v[42:43], v[42:43], v[52:53] op_sel_hi:[1,0]
	v_pk_mul_f32 v[44:45], v[44:45], v[52:53] op_sel_hi:[1,0]
	s_waitcnt vmcnt(6)
	v_pk_fma_f32 v[46:47], v[110:111], v[38:39], v[114:115]
	v_pk_fma_f32 v[48:49], v[108:109], v[40:41], v[112:113]
	v_pk_mul_f32 v[38:39], v[56:57], v[52:53] op_sel_hi:[1,0]
	v_pk_mul_f32 v[40:41], v[64:65], v[52:53] op_sel_hi:[1,0]
	v_pk_mul_f32 v[32:33], v[32:33], v[52:53] op_sel_hi:[1,0]
	v_pk_mul_f32 v[36:37], v[36:37], v[52:53] op_sel_hi:[1,0]
	v_pk_mul_f32 v[28:29], v[28:29], v[52:53] op_sel_hi:[1,0]
	s_waitcnt vmcnt(0)
	v_pk_fma_f32 v[52:53], v[134:135], v[26:27], v[138:139]
	v_max_f32_e64 v26, |v60|, |v61|
	v_max_f32_e64 v27, |v54|, |v55|
	v_pk_fma_f32 v[62:63], v[94:95], v[62:63], v[98:99]
	v_pk_fma_f32 v[50:51], v[92:93], v[50:51], v[96:97]
	v_pk_fma_f32 v[84:85], v[132:133], v[28:29], v[136:137]
	v_max3_f32 v26, v26, 0, v27
	v_max_f32_e64 v27, |v76|, |v77|
	v_max_f32_e64 v28, |v58|, |v59|
	v_pk_fma_f32 v[44:45], v[102:103], v[44:45], v[106:107]
	v_pk_fma_f32 v[78:79], v[100:101], v[42:43], v[104:105]
	v_max3_f32 v26, v26, v27, v28
	v_max_f32_e64 v27, |v50|, |v51|
	v_max_f32_e64 v28, |v62|, |v63|
	v_max3_f32 v26, v26, v27, v28
	v_max_f32_e64 v27, |v78|, |v79|
	v_max_f32_e64 v28, |v44|, |v45|
	v_pk_fma_f32 v[56:57], v[118:119], v[40:41], v[122:123]
	v_pk_fma_f32 v[64:65], v[116:117], v[38:39], v[120:121]
	v_max3_f32 v26, v26, v27, v28
	v_max_f32_e64 v27, |v48|, |v49|
	v_max_f32_e64 v28, |v46|, |v47|
	v_pk_fma_f32 v[80:81], v[126:127], v[36:37], v[130:131]
	v_pk_fma_f32 v[82:83], v[124:125], v[32:33], v[128:129]
	v_max3_f32 v26, v26, v27, v28
	v_max_f32_e64 v27, |v64|, |v65|
	v_max_f32_e64 v28, |v56|, |v57|
	v_max3_f32 v26, v26, v27, v28
	v_max_f32_e64 v27, |v82|, |v83|
	v_max_f32_e64 v28, |v80|, |v81|
	v_max3_f32 v26, v26, v27, v28
	v_max_f32_e64 v27, |v84|, |v85|
	v_max_f32_e64 v28, |v52|, |v53|
	v_max3_f32 v26, v26, v27, v28
	s_nop 1
	v_mov_b32_dpp v27, v26 quad_perm:[1,0,3,2] row_mask:0xf bank_mask:0xf
	s_cselect_b64 s[16:17], -1, 0
	s_cmpk_lt_i32 s6, 0x4000
	s_cselect_b32 s2, s6, s2
	s_ashr_i32 s3, s2, 31
	s_waitcnt lgkmcnt(0)
	v_max_f32_e32 v27, v27, v27
	v_max_f32_e32 v26, v26, v27
	s_nop 1
	v_mov_b32_dpp v27, v26 quad_perm:[2,3,0,1] row_mask:0xf bank_mask:0xf
	s_lshl_b64 s[2:3], s[2:3], 12
	v_lshl_add_u64 v[86:87], v[0:1], 0, s[2:3]
	s_waitcnt lgkmcnt(0)
	v_max_f32_e32 v27, v27, v27
	v_max_f32_e32 v26, v26, v27
	s_nop 1
	v_mov_b32_dpp v27, v26 row_half_mirror row_mask:0xf bank_mask:0xf
	s_waitcnt lgkmcnt(0)
	v_max_f32_e32 v27, v27, v27
	v_max_f32_e32 v26, v26, v27
	s_nop 1
	v_mov_b32_dpp v27, v26 row_mirror row_mask:0xf bank_mask:0xf
	s_waitcnt lgkmcnt(0)
	v_max_f32_e32 v27, v27, v27
	v_max_f32_e32 v26, v26, v27
	v_mov_b32_e32 v27, v26
	s_nop 1
	v_permlane16_swap_b32_e32 v27, v26
	s_waitcnt lgkmcnt(0)
	v_max_f32_e32 v27, v27, v27
	v_max_f32_e32 v28, v26, v27
	v_mov_b32_e32 v29, v28
	s_nop 1
	v_permlane32_swap_b32_e32 v29, v28
	global_load_dwordx2 v[34:35], v[86:87], off
	global_load_dwordx2 v[36:37], v[86:87], off offset:512
	global_load_dwordx2 v[38:39], v[86:87], off offset:1024
	global_load_dwordx2 v[26:27], v[86:87], off offset:1536
	s_waitcnt lgkmcnt(0)
	v_max_f32_e32 v29, v29, v29
	v_max_f32_e32 v42, v28, v29
	global_load_dwordx2 v[32:33], v[86:87], off offset:2048
	global_load_dwordx2 v[40:41], v[86:87], off offset:2560
	global_load_dwordx2 v[28:29], v[86:87], off offset:3072
	global_load_dwordx2 v[30:31], v[86:87], off offset:3584
	v_div_scale_f32 v43, s[2:3], v42, v42, s9
	v_rcp_f32_e32 v75, v43
	v_cvt_pk_bf16_f32 v90, v60, v61
	v_cvt_pk_bf16_f32 v91, v54, v55
	s_nop 0
	v_fma_f32 v86, -v43, v75, 1.0
	v_fmac_f32_e32 v75, v86, v75
	v_div_scale_f32 v86, vcc, s9, v42, s9
	v_mul_f32_e32 v87, v86, v75
	v_fma_f32 v88, -v43, v87, v86
	v_fmac_f32_e32 v87, v88, v75
	v_fma_f32 v43, -v43, v87, v86
	v_div_fmas_f32 v43, v43, v75, v87
	v_div_fixup_f32 v43, v43, v42, s9
	v_cmp_lt_f32_e32 vcc, 0, v42
	v_lshl_add_u64 v[86:87], s[66:67], 0, v[22:23]
	v_add_co_u32_e64 v86, s[2:3], s20, v86
	v_cndmask_b32_e32 v43, 0, v43, vcc
	v_fmaak_f32 v60, v60, v43, 0x4b400000
	v_fmaak_f32 v61, v61, v43, 0x4b400000
	v_fmaak_f32 v54, v54, v43, 0x4b400000
	v_fmaak_f32 v55, v55, v43, 0x4b400000
	v_lshl_add_u64 v[88:89], s[66:67], 0, v[24:25]
	v_addc_co_u32_e64 v87, s[2:3], 0, v87, s[2:3]
	v_perm_b32 v60, v61, v60, s21
	v_perm_b32 v54, v55, v54, s22
	v_or_b32_e32 v60, v54, v60
	v_add_co_u32_e64 v54, s[2:3], s23, v88
	global_store_dwordx2 v[86:87], v[90:91], off
	s_nop 0
	v_addc_co_u32_e64 v55, s[2:3], 0, v89, s[2:3]
	global_store_dword v[54:55], v60, off
	v_cvt_pk_bf16_f32 v60, v76, v77
	v_cvt_pk_bf16_f32 v61, v58, v59
	global_store_dwordx2 v[86:87], v[60:61], off offset:512
	v_fmaak_f32 v60, v76, v43, 0x4b400000
	v_fmaak_f32 v61, v77, v43, 0x4b400000
	v_fmaak_f32 v58, v58, v43, 0x4b400000
	v_fmaak_f32 v59, v59, v43, 0x4b400000
	v_perm_b32 v60, v61, v60, s21
	v_perm_b32 v58, v59, v58, s22
	v_or_b32_e32 v58, v58, v60
	global_store_dword v[54:55], v58, off offset:256
	v_cvt_pk_bf16_f32 v58, v50, v51
	v_cvt_pk_bf16_f32 v59, v62, v63
	global_store_dwordx2 v[86:87], v[58:59], off offset:1024
	v_fmaak_f32 v50, v50, v43, 0x4b400000
	v_fmaak_f32 v51, v51, v43, 0x4b400000
	v_fmaak_f32 v58, v62, v43, 0x4b400000
	v_fmaak_f32 v59, v63, v43, 0x4b400000
	v_perm_b32 v50, v51, v50, s21
	v_perm_b32 v51, v59, v58, s22
	v_or_b32_e32 v50, v51, v50
	global_store_dword v[54:55], v50, off offset:512
	v_cvt_pk_bf16_f32 v50, v78, v79
	v_cvt_pk_bf16_f32 v51, v44, v45
	global_store_dwordx2 v[86:87], v[50:51], off offset:1536
	v_fmaak_f32 v50, v78, v43, 0x4b400000
	v_fmaak_f32 v51, v79, v43, 0x4b400000
	v_fmaak_f32 v44, v44, v43, 0x4b400000
	v_fmaak_f32 v45, v45, v43, 0x4b400000
	v_perm_b32 v50, v51, v50, s21
	v_perm_b32 v44, v45, v44, s22
	v_or_b32_e32 v44, v44, v50
	global_store_dword v[54:55], v44, off offset:768
	v_cvt_pk_bf16_f32 v44, v48, v49
	v_cvt_pk_bf16_f32 v45, v46, v47
	global_store_dwordx2 v[86:87], v[44:45], off offset:2048
	v_fmaak_f32 v44, v48, v43, 0x4b400000
	v_fmaak_f32 v45, v49, v43, 0x4b400000
	v_fmaak_f32 v46, v46, v43, 0x4b400000
	v_fmaak_f32 v47, v47, v43, 0x4b400000
	v_perm_b32 v44, v45, v44, s21
	v_perm_b32 v45, v47, v46, s22
	v_or_b32_e32 v44, v45, v44
	global_store_dword v[54:55], v44, off offset:1024
	v_cvt_pk_bf16_f32 v44, v64, v65
	v_cvt_pk_bf16_f32 v45, v56, v57
	global_store_dwordx2 v[86:87], v[44:45], off offset:2560
	v_fmaak_f32 v44, v64, v43, 0x4b400000
	v_fmaak_f32 v45, v65, v43, 0x4b400000
	v_fmaak_f32 v46, v56, v43, 0x4b400000
	v_fmaak_f32 v47, v57, v43, 0x4b400000
	v_perm_b32 v44, v45, v44, s21
	v_perm_b32 v45, v47, v46, s22
	v_or_b32_e32 v44, v45, v44
	global_store_dword v[54:55], v44, off offset:1280
	v_cvt_pk_bf16_f32 v44, v82, v83
	v_cvt_pk_bf16_f32 v45, v80, v81
	global_store_dwordx2 v[86:87], v[44:45], off offset:3072
	v_fmaak_f32 v44, v82, v43, 0x4b400000
	v_fmaak_f32 v45, v83, v43, 0x4b400000
	v_fmaak_f32 v46, v80, v43, 0x4b400000
	v_fmaak_f32 v47, v81, v43, 0x4b400000
	v_perm_b32 v44, v45, v44, s21
	v_perm_b32 v45, v47, v46, s22
	v_or_b32_e32 v44, v45, v44
	global_store_dword v[54:55], v44, off offset:1536
	v_cvt_pk_bf16_f32 v44, v84, v85
	v_cvt_pk_bf16_f32 v45, v52, v53
	global_store_dwordx2 v[86:87], v[44:45], off offset:3584
	v_fmaak_f32 v44, v84, v43, 0x4b400000
	v_fmaak_f32 v45, v85, v43, 0x4b400000
	v_fmaak_f32 v46, v52, v43, 0x4b400000
	v_fmaak_f32 v43, v53, v43, 0x4b400000
	v_perm_b32 v44, v45, v44, s21
	v_perm_b32 v43, v43, v46, s22
	v_or_b32_e32 v43, v43, v44
	global_store_dword v[54:55], v43, off offset:1792
	s_and_saveexec_b64 s[2:3], s[0:1]
	s_cbranch_execz .LBB0_415
	s_add_u32 s24, s66, s18
	v_mul_f32_e32 v42, 0x3c010204, v42
	s_addc_u32 s25, s67, s19
	v_cndmask_b32_e32 v42, 1.0, v42, vcc
	global_store_dword v74, v42, s[24:25]
	s_branch .LBB0_415

.LBB0_1694:
	s_waitcnt vmcnt(23)
	v_mov_b64_e32 v[52:53], v[36:37]
	s_waitcnt vmcnt(22)
	v_mov_b64_e32 v[62:63], v[38:39]
	s_waitcnt lgkmcnt(0)
	v_lshlrev_b32_e32 v59, 16, v52
	v_lshlrev_b32_e32 v58, 16, v62
	v_and_b32_e32 v61, 0xffff0000, v52
	v_and_b32_e32 v60, 0xffff0000, v62
	v_lshlrev_b32_e32 v55, 16, v53
	v_lshlrev_b32_e32 v54, 16, v63
	v_and_b32_e32 v57, 0xffff0000, v53
	v_and_b32_e32 v56, 0xffff0000, v63
	v_pk_add_f32 v[52:53], v[58:59], v[60:61]
	v_pk_add_f32 v[62:63], v[54:55], v[56:57]
	s_waitcnt vmcnt(21)
	v_mov_b64_e32 v[64:65], v[40:41]
	v_pk_add_f32 v[52:53], v[52:53], v[62:63]
	s_waitcnt vmcnt(20)
	v_lshlrev_b32_e32 v46, 16, v29
	v_and_b32_e32 v47, 0xffff0000, v29
	v_add_f32_e32 v29, 0, v53
	v_add_f32_e32 v49, v52, v29
	v_lshlrev_b32_e32 v53, 16, v65
	v_lshlrev_b32_e32 v52, 16, v64
	v_and_b32_e32 v65, 0xffff0000, v65
	v_and_b32_e32 v64, 0xffff0000, v64
	v_pk_add_f32 v[62:63], v[52:53], v[64:65]
	v_lshlrev_b32_e32 v44, 16, v28
	v_and_b32_e32 v45, 0xffff0000, v28
	v_pk_add_f32 v[62:63], v[62:63], v[62:63] op_sel_hi:[0,1]
	s_waitcnt vmcnt(18)
	v_mov_b64_e32 v[66:67], v[42:43]
	v_lshlrev_b32_e32 v42, 16, v34
	v_and_b32_e32 v50, 0xffff0000, v34
	v_lshlrev_b32_e32 v40, 16, v35
	v_and_b32_e32 v48, 0xffff0000, v35
	v_add_f32_e32 v43, v44, v45
	v_add_f32_e32 v51, v46, v47
	v_mov_b32_e32 v41, v63
	v_pk_add_f32 v[68:69], v[42:43], v[50:51]
	v_pk_add_f32 v[62:63], v[40:41], v[48:49]
	v_lshlrev_b32_e32 v73, 16, v67
	v_lshlrev_b32_e32 v72, 16, v66
	v_and_b32_e32 v67, 0xffff0000, v67
	v_and_b32_e32 v66, 0xffff0000, v66
	v_pk_add_f32 v[62:63], v[68:69], v[62:63]
	v_pk_add_f32 v[68:69], v[72:73], v[66:67]
	s_waitcnt vmcnt(17)
	v_lshlrev_b32_e32 v34, 16, v32
	v_and_b32_e32 v35, 0xffff0000, v32
	v_lshlrev_b32_e32 v38, 16, v33
	v_and_b32_e32 v39, 0xffff0000, v33
	v_pk_add_f32 v[62:63], v[62:63], v[62:63] op_sel_hi:[0,1]
	v_pk_add_f32 v[68:69], v[68:69], v[68:69] op_sel_hi:[0,1]
	s_waitcnt vmcnt(16)
	v_lshlrev_b32_e32 v32, 16, v30
	v_and_b32_e32 v36, 0xffff0000, v30
	v_lshlrev_b32_e32 v28, 16, v31
	v_and_b32_e32 v30, 0xffff0000, v31
	v_add_f32_e32 v33, v34, v35
	v_add_f32_e32 v37, v38, v39
	v_mov_b32_e32 v29, v69
	v_mov_b32_e32 v31, v63
	v_pk_add_f32 v[70:71], v[32:33], v[36:37]
	v_pk_add_f32 v[62:63], v[28:29], v[30:31]
	s_nop 0
	v_pk_add_f32 v[62:63], v[70:71], v[62:63]
	s_nop 0
	v_add_f32_e32 v29, v62, v63
	s_nop 1
	v_mov_b32_dpp v31, v29 quad_perm:[1,0,3,2] row_mask:0xf bank_mask:0xf
	s_waitcnt lgkmcnt(0)
	v_add_f32_e32 v29, v29, v31
	s_nop 1
	v_mov_b32_dpp v31, v29 quad_perm:[2,3,0,1] row_mask:0xf bank_mask:0xf
	s_waitcnt lgkmcnt(0)
	v_add_f32_e32 v29, v29, v31
	s_nop 1
	v_mov_b32_dpp v31, v29 row_half_mirror row_mask:0xf bank_mask:0xf
	s_waitcnt lgkmcnt(0)
	v_add_f32_e32 v29, v29, v31
	s_nop 1
	v_mov_b32_dpp v31, v29 row_mirror row_mask:0xf bank_mask:0xf
	s_waitcnt lgkmcnt(0)
	v_add_f32_e32 v29, v29, v31
	v_mov_b32_e32 v31, v29
	s_nop 1
	v_permlane16_swap_b32_e32 v31, v29
	s_waitcnt lgkmcnt(0)
	v_add_f32_e32 v29, v29, v31
	v_mov_b32_e32 v31, v29
	s_nop 1
	v_permlane32_swap_b32_e32 v31, v29
	s_waitcnt lgkmcnt(0)
	v_add_f32_e32 v29, v29, v31
	v_fmac_f32_e32 v61, 0xba000000, v29
	v_fmac_f32_e32 v60, 0xba000000, v29
	v_fmac_f32_e32 v57, 0xba000000, v29
	v_fmac_f32_e32 v59, 0xba000000, v29
	v_fmac_f32_e32 v56, 0xba000000, v29
	v_fmac_f32_e32 v58, 0xba000000, v29
	v_mov_b32_e32 v68, v61
	v_mov_b32_e32 v69, v60
	v_fmac_f32_e32 v55, 0xba000000, v29
	v_fmac_f32_e32 v54, 0xba000000, v29
	v_mov_b32_e32 v62, v59
	v_mov_b32_e32 v63, v58
	v_pk_mul_f32 v[68:69], v[68:69], v[68:69]
	v_mov_b32_e32 v70, v57
	v_mov_b32_e32 v71, v56
	v_pk_fma_f32 v[62:63], v[62:63], v[62:63], v[68:69]
	v_mov_b32_e32 v68, v55
	v_mov_b32_e32 v69, v54
	v_pk_mul_f32 v[70:71], v[70:71], v[70:71]
	v_fmac_f32_e32 v64, 0xba000000, v29
	v_pk_fma_f32 v[68:69], v[68:69], v[68:69], v[70:71]
	v_fmac_f32_e32 v65, 0xba000000, v29
	v_pk_add_f32 v[62:63], v[62:63], v[68:69]
	v_fmac_f32_e32 v53, 0xba000000, v29
	v_pk_add_f32 v[68:69], v[62:63], v[62:63] op_sel_hi:[0,1]
	v_fmac_f32_e32 v52, 0xba000000, v29
	v_mov_b32_e32 v62, v53
	v_mov_b32_e32 v63, v65
	v_mov_b32_e32 v53, v64
	v_pk_mul_f32 v[70:71], v[62:63], v[62:63]
	v_pk_mul_f32 v[64:65], v[52:53], v[52:53]
	v_fmac_f32_e32 v44, 0xba000000, v29
	v_pk_mov_b32 v[74:75], v[64:65], v[70:71] op_sel:[1,0]
	v_mov_b32_e32 v65, v71
	v_pk_add_f32 v[64:65], v[74:75], v[64:65]
	v_fmac_f32_e32 v45, 0xba000000, v29
	v_pk_add_f32 v[64:65], v[64:65], v[64:65] op_sel_hi:[0,1]
	v_fmac_f32_e32 v46, 0xba000000, v29
	v_mul_f32_e32 v64, v44, v44
	v_fmac_f32_e32 v47, 0xba000000, v29
	v_pk_fma_f32 v[70:71], v[44:45], v[44:45], v[64:65] op_sel_hi:[1,1,0]
	v_mul_f32_e32 v64, v46, v46
	v_pk_fma_f32 v[74:75], v[46:47], v[46:47], v[64:65] op_sel_hi:[1,1,0]
	v_fmac_f32_e32 v48, 0xba000000, v29
	v_fmac_f32_e32 v40, 0xba000000, v29
	v_fmac_f32_e32 v50, 0xba000000, v29
	v_fmac_f32_e32 v42, 0xba000000, v29
	v_mul_f32_e32 v70, v42, v42
	v_mul_f32_e32 v74, v50, v50
	v_mul_f32_e32 v64, v40, v40
	v_mul_f32_e32 v68, v48, v48
	v_pk_add_f32 v[70:71], v[70:71], v[74:75]
	v_pk_add_f32 v[64:65], v[64:65], v[68:69]
	v_fmac_f32_e32 v66, 0xba000000, v29
	v_fmac_f32_e32 v67, 0xba000000, v29
	v_fmac_f32_e32 v73, 0xba000000, v29
	v_pk_add_f32 v[64:65], v[70:71], v[64:65]
	v_fmac_f32_e32 v72, 0xba000000, v29
	v_mov_b32_e32 v78, v73
	v_mov_b32_e32 v79, v67
	v_mov_b32_e32 v73, v66
	v_pk_add_f32 v[64:65], v[64:65], v[64:65] op_sel_hi:[0,1]
	v_pk_mul_f32 v[68:69], v[78:79], v[78:79]
	v_pk_mul_f32 v[66:67], v[72:73], v[72:73]
	v_fmac_f32_e32 v34, 0xba000000, v29
	v_pk_mov_b32 v[70:71], v[66:67], v[68:69] op_sel:[1,0]
	v_mov_b32_e32 v67, v69
	v_fmac_f32_e32 v35, 0xba000000, v29
	v_fmac_f32_e32 v38, 0xba000000, v29
	v_mul_f32_e32 v64, v34, v34
	v_pk_add_f32 v[66:67], v[70:71], v[66:67]
	v_fmac_f32_e32 v39, 0xba000000, v29
	v_pk_fma_f32 v[68:69], v[34:35], v[34:35], v[64:65] op_sel_hi:[1,1,0]
	v_mul_f32_e32 v64, v38, v38
	v_pk_add_f32 v[66:67], v[66:67], v[66:67] op_sel_hi:[0,1]
	v_pk_fma_f32 v[70:71], v[38:39], v[38:39], v[64:65] op_sel_hi:[1,1,0]
	v_fmac_f32_e32 v30, 0xba000000, v29
	v_fmac_f32_e32 v28, 0xba000000, v29
	v_fmac_f32_e32 v36, 0xba000000, v29
	v_fmac_f32_e32 v32, 0xba000000, v29
	v_mul_f32_e32 v68, v32, v32
	v_mul_f32_e32 v70, v36, v36
	v_mul_f32_e32 v66, v28, v28
	v_mul_f32_e32 v64, v30, v30
	v_pk_add_f32 v[68:69], v[68:69], v[70:71]
	v_pk_add_f32 v[64:65], v[66:67], v[64:65]
	v_mov_b32_e32 v151, v60
	v_pk_add_f32 v[64:65], v[68:69], v[64:65]
	v_mov_b32_e32 v60, v59
	v_add_f32_e32 v29, v64, v65
	global_load_dwordx4 v[64:67], v[4:5], off
	global_load_dwordx4 v[68:71], v[6:7], off
	global_load_dwordx4 v[94:97], v[4:5], off offset:1024
	global_load_dwordx4 v[98:101], v[6:7], off offset:1024
	global_load_dwordx4 v[102:105], v[4:5], off offset:2048
	global_load_dwordx4 v[106:109], v[6:7], off offset:2048
	global_load_dwordx4 v[110:113], v[4:5], off offset:3072
	global_load_dwordx4 v[114:117], v[6:7], off offset:3072
	global_load_dwordx4 v[118:121], v[8:9], off
	global_load_dwordx4 v[122:125], v[10:11], off
	global_load_dwordx4 v[126:129], v[12:13], off
	global_load_dwordx4 v[130:133], v[14:15], off
	global_load_dwordx4 v[134:137], v[16:17], off
	global_load_dwordx4 v[138:141], v[18:19], off
	global_load_dwordx4 v[142:145], v[20:21], off
	global_load_dwordx4 v[146:149], v[22:23], off
	s_nop 1
	v_mov_b32_dpp v31, v29 quad_perm:[1,0,3,2] row_mask:0xf bank_mask:0xf
	v_mov_b32_e32 v59, v56
	v_mov_b32_e32 v56, v55
	v_mov_b32_e32 v150, v58
	v_mov_b32_e32 v58, v54
	s_waitcnt lgkmcnt(0)
	v_add_f32_e32 v29, v29, v31
	s_nop 1
	v_mov_b32_dpp v31, v29 quad_perm:[2,3,0,1] row_mask:0xf bank_mask:0xf
	s_waitcnt lgkmcnt(0)
	v_add_f32_e32 v29, v29, v31
	s_nop 1
	v_mov_b32_dpp v31, v29 row_half_mirror row_mask:0xf bank_mask:0xf
	s_waitcnt lgkmcnt(0)
	v_add_f32_e32 v29, v29, v31
	s_nop 1
	v_mov_b32_dpp v31, v29 row_mirror row_mask:0xf bank_mask:0xf
	s_waitcnt lgkmcnt(0)
	v_add_f32_e32 v29, v29, v31
	v_mov_b32_e32 v31, v29
	s_nop 1
	v_permlane16_swap_b32_e32 v31, v29
	s_waitcnt lgkmcnt(0)
	v_add_f32_e32 v29, v29, v31
	v_mov_b32_e32 v31, v29
	s_nop 1
	v_permlane32_swap_b32_e32 v31, v29
	s_waitcnt lgkmcnt(0)
	v_add_f32_e32 v29, v29, v31
	v_fmamk_f32 v29, v29, 0x3a000000, v89
	v_mul_f32_e32 v31, 0x4f800000, v29
	v_cmp_gt_f32_e32 vcc, s39, v29
	s_nop 1
	v_cndmask_b32_e32 v29, v29, v31, vcc
	v_sqrt_f32_e32 v31, v29
	s_nop 0
	v_add_u32_e32 v33, -1, v31
	v_fma_f32 v37, -v33, v31, v29
	v_cmp_ge_f32_e64 s[2:3], 0, v37
	v_add_u32_e32 v37, 1, v31
	s_nop 0
	v_cndmask_b32_e64 v33, v31, v33, s[2:3]
	v_fma_f32 v31, -v37, v31, v29
	v_cmp_lt_f32_e64 s[2:3], 0, v31
	s_nop 1
	v_cndmask_b32_e64 v31, v33, v37, s[2:3]
	v_mul_f32_e32 v33, 0x37800000, v31
	v_cndmask_b32_e32 v31, v31, v33, vcc
	v_cmp_class_f32_e32 vcc, v29, v90
	s_nop 1
	v_cndmask_b32_e32 v29, v31, v29, vcc
	v_div_scale_f32 v31, s[2:3], v29, v29, 1.0
	v_rcp_f32_e32 v33, v31
	s_mov_b32 s2, s18
	s_add_i32 s18, s18, 8
	s_cmp_ge_i32 s18, s34
	v_fma_f32 v37, -v31, v33, 1.0
	v_fmac_f32_e32 v33, v37, v33
	v_div_scale_f32 v37, vcc, 1.0, v29, 1.0
	v_mul_f32_e32 v41, v37, v33
	v_fma_f32 v43, -v31, v41, v37
	v_fmac_f32_e32 v41, v43, v33
	v_fma_f32 v31, -v31, v41, v37
	v_div_fmas_f32 v31, v31, v33, v41
	v_div_fixup_f32 v152, v31, v29, 1.0
	v_pk_mul_f32 v[54:55], v[60:61], v[152:153] op_sel_hi:[1,0]
	v_pk_mul_f32 v[56:57], v[56:57], v[152:153] op_sel_hi:[1,0]
	v_mov_b32_e32 v29, v30
	s_waitcnt vmcnt(14)
	v_pk_fma_f32 v[74:75], v[66:67], v[56:57], v[70:71]
	v_pk_fma_f32 v[76:77], v[64:65], v[54:55], v[68:69]
	v_pk_mul_f32 v[54:55], v[150:151], v[152:153] op_sel_hi:[1,0]
	v_pk_mul_f32 v[56:57], v[58:59], v[152:153] op_sel_hi:[1,0]
	v_pk_mul_f32 v[44:45], v[44:45], v[152:153] op_sel_hi:[1,0]
	v_pk_mul_f32 v[28:29], v[28:29], v[152:153] op_sel_hi:[1,0]
	s_waitcnt vmcnt(12)
	v_pk_fma_f32 v[66:67], v[96:97], v[56:57], v[100:101]
	v_pk_fma_f32 v[70:71], v[94:95], v[54:55], v[98:99]
	v_pk_mul_f32 v[52:53], v[52:53], v[152:153] op_sel_hi:[1,0]
	v_pk_mul_f32 v[54:55], v[62:63], v[152:153] op_sel_hi:[1,0]
	s_waitcnt vmcnt(8)
	v_pk_fma_f32 v[64:65], v[110:111], v[44:45], v[114:115]
	s_waitcnt vmcnt(0)
	v_pk_fma_f32 v[44:45], v[144:145], v[28:29], v[148:149]
	v_max_f32_e64 v28, |v76|, |v77|
	v_max_f32_e64 v29, |v74|, |v75|
	v_pk_fma_f32 v[62:63], v[104:105], v[54:55], v[108:109]
	v_pk_fma_f32 v[68:69], v[102:103], v[52:53], v[106:107]
	v_pk_mul_f32 v[46:47], v[46:47], v[152:153] op_sel_hi:[1,0]
	v_mov_b32_e32 v43, v50
	v_mov_b32_e32 v41, v48
	v_max3_f32 v28, v28, 0, v29
	v_max_f32_e64 v29, |v70|, |v71|
	v_max_f32_e64 v30, |v66|, |v67|
	v_pk_fma_f32 v[60:61], v[112:113], v[46:47], v[116:117]
	v_pk_mul_f32 v[42:43], v[42:43], v[152:153] op_sel_hi:[1,0]
	v_pk_mul_f32 v[40:41], v[40:41], v[152:153] op_sel_hi:[1,0]
	v_max3_f32 v28, v28, v29, v30
	v_max_f32_e64 v29, |v68|, |v69|
	v_max_f32_e64 v30, |v62|, |v63|
	v_pk_fma_f32 v[54:55], v[120:121], v[40:41], v[124:125]
	v_pk_fma_f32 v[58:59], v[118:119], v[42:43], v[122:123]
	v_pk_mul_f32 v[40:41], v[72:73], v[152:153] op_sel_hi:[1,0]
	v_pk_mul_f32 v[42:43], v[78:79], v[152:153] op_sel_hi:[1,0]
	v_max3_f32 v28, v28, v29, v30
	v_max_f32_e64 v29, |v64|, |v65|
	v_max_f32_e64 v30, |v60|, |v61|
	v_pk_fma_f32 v[52:53], v[128:129], v[42:43], v[132:133]
	v_pk_fma_f32 v[56:57], v[126:127], v[40:41], v[130:131]
	v_pk_mul_f32 v[34:35], v[34:35], v[152:153] op_sel_hi:[1,0]
	v_pk_mul_f32 v[38:39], v[38:39], v[152:153] op_sel_hi:[1,0]
	v_mov_b32_e32 v33, v36
	v_max3_f32 v28, v28, v29, v30
	v_max_f32_e64 v29, |v58|, |v59|
	v_max_f32_e64 v30, |v54|, |v55|
	v_pk_fma_f32 v[46:47], v[136:137], v[38:39], v[140:141]
	v_pk_fma_f32 v[50:51], v[134:135], v[34:35], v[138:139]
	v_pk_mul_f32 v[32:33], v[32:33], v[152:153] op_sel_hi:[1,0]
	v_max3_f32 v28, v28, v29, v30
	v_max_f32_e64 v29, |v56|, |v57|
	v_max_f32_e64 v30, |v52|, |v53|
	v_pk_fma_f32 v[48:49], v[142:143], v[32:33], v[146:147]
	v_max3_f32 v28, v28, v29, v30
	v_max_f32_e64 v29, |v50|, |v51|
	v_max_f32_e64 v30, |v46|, |v47|
	v_max3_f32 v28, v28, v29, v30
	v_max_f32_e64 v29, |v48|, |v49|
	v_max_f32_e64 v30, |v44|, |v45|
	v_max3_f32 v28, v28, v29, v30
	s_nop 1
	v_mov_b32_dpp v29, v28 quad_perm:[1,0,3,2] row_mask:0xf bank_mask:0xf
	s_cselect_b64 s[28:29], -1, 0
	s_cmp_lt_i32 s18, s34
	s_cselect_b32 s2, s18, s2
	s_ashr_i32 s3, s2, 31
	s_waitcnt lgkmcnt(0)
	v_max_f32_e32 v29, v29, v29
	v_max_f32_e32 v28, v28, v29
	s_nop 1
	v_mov_b32_dpp v29, v28 quad_perm:[2,3,0,1] row_mask:0xf bank_mask:0xf
	s_lshl_b64 s[2:3], s[2:3], 12
	v_lshl_add_u64 v[30:31], v[2:3], 0, s[2:3]
	s_waitcnt lgkmcnt(0)
	v_max_f32_e32 v29, v29, v29
	v_max_f32_e32 v28, v28, v29
	s_nop 1
	v_mov_b32_dpp v29, v28 row_half_mirror row_mask:0xf bank_mask:0xf
	s_waitcnt lgkmcnt(0)
	v_max_f32_e32 v29, v29, v29
	v_max_f32_e32 v28, v28, v29
	s_nop 1
	v_mov_b32_dpp v29, v28 row_mirror row_mask:0xf bank_mask:0xf
	s_waitcnt lgkmcnt(0)
	v_max_f32_e32 v29, v29, v29
	v_max_f32_e32 v28, v28, v29
	v_mov_b32_e32 v29, v28
	s_nop 1
	v_permlane16_swap_b32_e32 v29, v28
	s_waitcnt lgkmcnt(0)
	v_max_f32_e32 v29, v29, v29
	v_max_f32_e32 v32, v28, v29
	v_mov_b32_e32 v33, v32
	s_nop 1
	v_permlane32_swap_b32_e32 v33, v32
	global_load_dwordx2 v[36:37], v[30:31], off
	global_load_dwordx2 v[38:39], v[30:31], off offset:512
	global_load_dwordx2 v[40:41], v[30:31], off offset:1024
	global_load_dwordx2 v[28:29], v[30:31], off offset:1536
	s_waitcnt lgkmcnt(0)
	v_max_f32_e32 v33, v33, v33
	v_max_f32_e32 v72, v32, v33
	global_load_dwordx2 v[34:35], v[30:31], off offset:2048
	global_load_dwordx2 v[42:43], v[30:31], off offset:2560
	global_load_dwordx2 v[32:33], v[30:31], off offset:3072
	s_nop 0
	global_load_dwordx2 v[30:31], v[30:31], off offset:3584
	v_div_scale_f32 v73, s[2:3], v72, v72, s40
	v_rcp_f32_e32 v78, v73
	s_nop 0
	v_fma_f32 v79, -v73, v78, 1.0
	v_fmac_f32_e32 v78, v79, v78
	v_div_scale_f32 v79, vcc, s40, v72, s40
	v_mul_f32_e32 v94, v79, v78
	v_fma_f32 v95, -v73, v94, v79
	v_fmac_f32_e32 v94, v95, v78
	v_fma_f32 v73, -v73, v94, v79
	v_div_fmas_f32 v73, v73, v78, v94
	v_div_fixup_f32 v73, v73, v72, s40
	v_cmp_lt_f32_e32 vcc, 0, v72
	v_cvt_pk_bf16_f32 v78, v76, v77
	v_cvt_pk_bf16_f32 v79, v74, v75
	global_store_dwordx2 v[26:27], v[78:79], off offset:-2048
	s_nop 0
	v_cndmask_b32_e32 v73, 0, v73, vcc
	v_fmaak_f32 v78, v76, v73, 0x4b400000
	v_fmaak_f32 v79, v77, v73, 0x4b400000
	v_fmaak_f32 v94, v74, v73, 0x4b400000
	v_fmaak_f32 v95, v75, v73, 0x4b400000
	v_perm_b32 v78, v79, v78, s41
	v_perm_b32 v79, v95, v94, s42
	v_or_b32_e32 v78, v79, v78
	global_store_dword v[24:25], v78, off offset:-1024
	v_cvt_pk_bf16_f32 v78, v70, v71
	v_cvt_pk_bf16_f32 v79, v66, v67
	global_store_dwordx2 v[26:27], v[78:79], off offset:-1536
	v_fmaak_f32 v78, v70, v73, 0x4b400000
	v_fmaak_f32 v79, v71, v73, 0x4b400000
	v_fmaak_f32 v94, v66, v73, 0x4b400000
	v_fmaak_f32 v95, v67, v73, 0x4b400000
	v_perm_b32 v78, v79, v78, s41
	v_perm_b32 v79, v95, v94, s42
	v_or_b32_e32 v78, v79, v78
	global_store_dword v[24:25], v78, off offset:-768
	v_cvt_pk_bf16_f32 v78, v68, v69
	v_cvt_pk_bf16_f32 v79, v62, v63
	global_store_dwordx2 v[26:27], v[78:79], off offset:-1024
	v_fmaak_f32 v78, v68, v73, 0x4b400000
	v_fmaak_f32 v79, v69, v73, 0x4b400000
	v_fmaak_f32 v94, v62, v73, 0x4b400000
	v_fmaak_f32 v95, v63, v73, 0x4b400000
	v_perm_b32 v78, v79, v78, s41
	v_perm_b32 v79, v95, v94, s42
	v_or_b32_e32 v78, v79, v78
	global_store_dword v[24:25], v78, off offset:-512
	v_cvt_pk_bf16_f32 v78, v64, v65
	v_cvt_pk_bf16_f32 v79, v60, v61
	global_store_dwordx2 v[26:27], v[78:79], off offset:-512
	v_fmaak_f32 v78, v64, v73, 0x4b400000
	v_fmaak_f32 v79, v65, v73, 0x4b400000
	v_fmaak_f32 v94, v60, v73, 0x4b400000
	v_fmaak_f32 v95, v61, v73, 0x4b400000
	v_perm_b32 v78, v79, v78, s41
	v_perm_b32 v79, v95, v94, s42
	v_or_b32_e32 v78, v79, v78
	global_store_dword v[24:25], v78, off offset:-256
	v_cvt_pk_bf16_f32 v78, v58, v59
	v_cvt_pk_bf16_f32 v79, v54, v55
	global_store_dwordx2 v[26:27], v[78:79], off
	v_fmaak_f32 v78, v58, v73, 0x4b400000
	v_fmaak_f32 v79, v59, v73, 0x4b400000
	v_fmaak_f32 v94, v54, v73, 0x4b400000
	v_fmaak_f32 v95, v55, v73, 0x4b400000
	v_perm_b32 v78, v79, v78, s41
	v_perm_b32 v79, v95, v94, s42
	v_or_b32_e32 v78, v79, v78
	global_store_dword v[24:25], v78, off
	v_cvt_pk_bf16_f32 v78, v56, v57
	v_cvt_pk_bf16_f32 v79, v52, v53
	global_store_dwordx2 v[26:27], v[78:79], off offset:512
	v_fmaak_f32 v78, v56, v73, 0x4b400000
	v_fmaak_f32 v79, v57, v73, 0x4b400000
	v_fmaak_f32 v94, v52, v73, 0x4b400000
	v_fmaak_f32 v95, v53, v73, 0x4b400000
	v_perm_b32 v78, v79, v78, s41
	v_perm_b32 v79, v95, v94, s42
	v_or_b32_e32 v78, v79, v78
	global_store_dword v[24:25], v78, off offset:256
	v_cvt_pk_bf16_f32 v78, v50, v51
	v_cvt_pk_bf16_f32 v79, v46, v47
	global_store_dwordx2 v[26:27], v[78:79], off offset:1024
	v_fmaak_f32 v78, v50, v73, 0x4b400000
	v_fmaak_f32 v79, v51, v73, 0x4b400000
	v_fmaak_f32 v94, v46, v73, 0x4b400000
	v_fmaak_f32 v95, v47, v73, 0x4b400000
	v_perm_b32 v78, v79, v78, s41
	v_perm_b32 v79, v95, v94, s42
	v_or_b32_e32 v78, v79, v78
	global_store_dword v[24:25], v78, off offset:512
	v_cvt_pk_bf16_f32 v78, v48, v49
	v_cvt_pk_bf16_f32 v79, v44, v45
	global_store_dwordx2 v[26:27], v[78:79], off offset:1536
	v_fmaak_f32 v78, v48, v73, 0x4b400000
	v_fmaak_f32 v79, v49, v73, 0x4b400000
	v_fmaak_f32 v94, v44, v73, 0x4b400000
	v_fmaak_f32 v73, v45, v73, 0x4b400000
	v_perm_b32 v78, v79, v78, s41
	v_perm_b32 v73, v73, v94, s42
	v_or_b32_e32 v73, v73, v78
	global_store_dword v[24:25], v73, off offset:768
	s_and_saveexec_b64 s[2:3], s[0:1]
	s_cbranch_execz .LBB0_1696
	v_mul_f32_e32 v72, 0x3c010204, v72
	v_cndmask_b32_e32 v72, 1.0, v72, vcc
	global_store_dword v91, v72, s[22:23]

.LBB0_1993:
	s_add_i32 s14, s24, s26
	s_cmpk_gt_i32 s14, 0x3fff
	s_cbranch_scc1 .LBB0_1992
	s_ashr_i32 s9, s8, 31
	s_lshl_b64 s[2:3], s[8:9], 2
	s_add_u32 s16, s20, s2
	s_addc_u32 s17, s21, s3
	global_load_dwordx2 v[26:27], v58, s[16:17]
	s_waitcnt vmcnt(0)
	v_readfirstlane_b32 s18, v26
	v_readfirstlane_b32 s16, v27
	s_max_i32 s9, s18, s16
	s_cmp_ge_i32 s9, s27
	s_cbranch_scc1 .LBB0_1992
	s_ashr_i32 s15, s14, 31
	s_add_u32 s2, s11, s2
	s_addc_u32 s3, s13, s3
	s_lshl_b64 s[34:35], s[14:15], 12
	v_lshl_add_u64 v[28:29], v[22:23], 0, s[34:35]
	global_load_dwordx2 v[26:27], v[28:29], off
	global_load_dwordx2 v[30:31], v[28:29], off offset:512
	global_load_dwordx2 v[32:33], v[28:29], off offset:1024
	s_ashr_i32 s19, s18, 31
	s_ashr_i32 s17, s16, 31
	s_lshl_b64 s[18:19], s[18:19], 12
	s_lshl_b64 s[16:17], s[16:17], 12
	v_lshl_add_u64 v[34:35], v[24:25], 0, s[18:19]
	v_lshl_add_u64 v[38:39], v[24:25], 0, s[16:17]
	global_load_dwordx2 v[36:37], v[34:35], off
	global_load_dwordx2 v[40:41], v[38:39], off
	global_load_dwordx2 v[42:43], v[34:35], off offset:512
	global_load_dwordx2 v[44:45], v[38:39], off offset:512
	global_load_dwordx2 v[46:47], v[34:35], off offset:1024
	global_load_dwordx2 v[48:49], v[38:39], off offset:1024
	global_load_dwordx2 v[56:57], v58, s[2:3]
	global_load_dwordx2 v[50:51], v[28:29], off offset:1536
	global_load_dwordx2 v[52:53], v[34:35], off offset:1536
	global_load_dwordx2 v[54:55], v[38:39], off offset:1536
	global_load_dwordx2 v[70:71], v[28:29], off offset:2048
	global_load_dwordx2 v[72:73], v[28:29], off offset:2560
	global_load_dwordx2 v[74:75], v[28:29], off offset:3072
	global_load_dwordx2 v[76:77], v[34:35], off offset:2048
	global_load_dwordx2 v[78:79], v[34:35], off offset:2560
	global_load_dwordx2 v[80:81], v[34:35], off offset:3072
	global_load_dwordx2 v[82:83], v[38:39], off offset:2048
	global_load_dwordx2 v[84:85], v[38:39], off offset:2560
	global_load_dwordx2 v[86:87], v[38:39], off offset:3072
	global_load_dwordx2 v[88:89], v[28:29], off offset:3584
	global_load_dwordx2 v[90:91], v[34:35], off offset:3584
	v_cmp_lt_i32_e32 vcc, v64, v63
	s_waitcnt vmcnt(19)
	v_lshlrev_b32_e32 v96, 16, v40
	s_waitcnt vmcnt(18)
	v_lshlrev_b32_e32 v98, 16, v42
	v_and_b32_e32 v99, 0xffff0000, v42
	v_lshlrev_b32_e32 v42, 16, v43
	v_and_b32_e32 v43, 0xffff0000, v43
	s_waitcnt vmcnt(16)
	v_lshlrev_b32_e32 v102, 16, v46
	v_and_b32_e32 v103, 0xffff0000, v46
	s_waitcnt vmcnt(14)
	v_pk_mul_f32 v[42:43], v[56:57], v[42:43] op_sel_hi:[0,1]
	v_pk_mul_f32 v[102:103], v[56:57], v[102:103] op_sel_hi:[0,1]
	v_and_b32_e32 v97, 0xffff0000, v40
	v_lshlrev_b32_e32 v28, 16, v26
	v_lshlrev_b32_e32 v34, 16, v30
	v_and_b32_e32 v35, 0xffff0000, v30
	v_lshlrev_b32_e32 v30, 16, v31
	v_and_b32_e32 v31, 0xffff0000, v31
	v_lshlrev_b32_e32 v92, 16, v32
	v_and_b32_e32 v93, 0xffff0000, v32
	v_pk_fma_f32 v[30:31], v[30:31], s[12:13], v[42:43] op_sel_hi:[1,0,1]
	v_pk_fma_f32 v[42:43], v[92:93], s[12:13], v[102:103] op_sel_hi:[1,0,1]
	global_load_dwordx2 v[92:93], v[38:39], off offset:3584
	v_lshlrev_b32_e32 v94, 16, v36
	v_and_b32_e32 v95, 0xffff0000, v36
	v_and_b32_e32 v29, 0xffff0000, v26
	v_lshlrev_b32_e32 v36, 16, v37
	v_and_b32_e32 v37, 0xffff0000, v37
	v_pk_mul_f32 v[94:95], v[56:57], v[94:95] op_sel_hi:[0,1]
	v_lshlrev_b32_e32 v26, 16, v27
	v_and_b32_e32 v27, 0xffff0000, v27
	v_lshlrev_b32_e32 v100, 16, v44
	v_and_b32_e32 v101, 0xffff0000, v44
	v_lshlrev_b32_e32 v44, 16, v45
	v_and_b32_e32 v45, 0xffff0000, v45
	v_lshlrev_b32_e32 v46, 16, v47
	v_and_b32_e32 v47, 0xffff0000, v47
	v_lshlrev_b32_e32 v104, 16, v48
	v_and_b32_e32 v105, 0xffff0000, v48
	v_pk_mul_f32 v[36:37], v[56:57], v[36:37] op_sel_hi:[0,1]
	v_pk_fma_f32 v[28:29], v[28:29], s[12:13], v[94:95] op_sel_hi:[1,0,1]
	v_lshlrev_b32_e32 v32, 16, v33
	v_and_b32_e32 v33, 0xffff0000, v33
	v_lshlrev_b32_e32 v40, 16, v41
	v_and_b32_e32 v41, 0xffff0000, v41
	v_pk_mul_f32 v[46:47], v[56:57], v[46:47] op_sel_hi:[0,1]
	v_pk_fma_f32 v[26:27], v[26:27], s[12:13], v[36:37] op_sel_hi:[1,0,1]
	v_pk_fma_f32 v[36:37], v[56:57], v[96:97], v[28:29] op_sel:[1,0,0]
	v_pk_fma_f32 v[30:31], v[56:57], v[44:45], v[30:31] op_sel:[1,0,0]
	v_pk_fma_f32 v[28:29], v[56:57], v[104:105], v[42:43] op_sel:[1,0,0]
	s_waitcnt vmcnt(13)
	v_lshlrev_b32_e32 v42, 16, v52
	v_and_b32_e32 v43, 0xffff0000, v52
	v_lshlrev_b32_e32 v44, 16, v53
	v_and_b32_e32 v45, 0xffff0000, v53
	v_lshlrev_b32_e32 v48, 16, v49
	v_and_b32_e32 v49, 0xffff0000, v49
	v_pk_fma_f32 v[46:47], v[32:33], s[12:13], v[46:47] op_sel_hi:[1,0,1]
	v_pk_fma_f32 v[32:33], v[56:57], v[40:41], v[26:27] op_sel:[1,0,0]
	v_lshlrev_b32_e32 v40, 16, v50
	v_and_b32_e32 v41, 0xffff0000, v50
	v_lshlrev_b32_e32 v38, 16, v51
	v_and_b32_e32 v39, 0xffff0000, v51
	v_pk_mul_f32 v[44:45], v[56:57], v[44:45] op_sel_hi:[0,1]
	v_pk_mul_f32 v[42:43], v[56:57], v[42:43] op_sel_hi:[0,1]
	v_pk_fma_f32 v[26:27], v[56:57], v[48:49], v[46:47] op_sel:[1,0,0]
	s_waitcnt vmcnt(12)
	v_lshlrev_b32_e32 v46, 16, v54
	v_and_b32_e32 v47, 0xffff0000, v54
	v_lshlrev_b32_e32 v48, 16, v55
	v_and_b32_e32 v49, 0xffff0000, v55
	v_pk_fma_f32 v[40:41], v[40:41], s[12:13], v[42:43] op_sel_hi:[1,0,1]
	v_pk_fma_f32 v[38:39], v[38:39], s[12:13], v[44:45] op_sel_hi:[1,0,1]
	v_pk_fma_f32 v[40:41], v[56:57], v[46:47], v[40:41] op_sel:[1,0,0]
	v_pk_fma_f32 v[38:39], v[56:57], v[48:49], v[38:39] op_sel:[1,0,0]
	s_waitcnt vmcnt(8)
	v_lshlrev_b32_e32 v46, 16, v76
	v_and_b32_e32 v47, 0xffff0000, v76
	v_lshlrev_b32_e32 v48, 16, v77
	v_and_b32_e32 v49, 0xffff0000, v77
	v_lshlrev_b32_e32 v42, 16, v70
	v_and_b32_e32 v43, 0xffff0000, v70
	v_lshlrev_b32_e32 v44, 16, v71
	v_and_b32_e32 v45, 0xffff0000, v71
	v_pk_mul_f32 v[48:49], v[56:57], v[48:49] op_sel_hi:[0,1]
	v_pk_mul_f32 v[46:47], v[56:57], v[46:47] op_sel_hi:[0,1]
	s_waitcnt vmcnt(5)
	v_lshlrev_b32_e32 v50, 16, v82
	v_and_b32_e32 v51, 0xffff0000, v82
	v_lshlrev_b32_e32 v52, 16, v83
	v_and_b32_e32 v53, 0xffff0000, v83
	v_pk_fma_f32 v[46:47], v[42:43], s[12:13], v[46:47] op_sel_hi:[1,0,1]
	v_pk_fma_f32 v[42:43], v[44:45], s[12:13], v[48:49] op_sel_hi:[1,0,1]
	v_pk_fma_f32 v[44:45], v[56:57], v[50:51], v[46:47] op_sel:[1,0,0]
	v_pk_fma_f32 v[42:43], v[56:57], v[52:53], v[42:43] op_sel:[1,0,0]
	v_lshlrev_b32_e32 v50, 16, v78
	v_and_b32_e32 v51, 0xffff0000, v78
	v_lshlrev_b32_e32 v52, 16, v79
	v_and_b32_e32 v53, 0xffff0000, v79
	v_lshlrev_b32_e32 v46, 16, v72
	v_and_b32_e32 v47, 0xffff0000, v72
	v_lshlrev_b32_e32 v48, 16, v73
	v_and_b32_e32 v49, 0xffff0000, v73
	v_pk_mul_f32 v[52:53], v[56:57], v[52:53] op_sel_hi:[0,1]
	v_pk_mul_f32 v[50:51], v[56:57], v[50:51] op_sel_hi:[0,1]
	s_waitcnt vmcnt(4)
	v_lshlrev_b32_e32 v54, 16, v84
	v_and_b32_e32 v55, 0xffff0000, v84
	v_lshlrev_b32_e32 v70, 16, v85
	v_and_b32_e32 v71, 0xffff0000, v85
	v_pk_fma_f32 v[50:51], v[46:47], s[12:13], v[50:51] op_sel_hi:[1,0,1]
	v_pk_fma_f32 v[46:47], v[48:49], s[12:13], v[52:53] op_sel_hi:[1,0,1]
	v_pk_fma_f32 v[48:49], v[56:57], v[54:55], v[50:51] op_sel:[1,0,0]
	v_pk_fma_f32 v[46:47], v[56:57], v[70:71], v[46:47] op_sel:[1,0,0]
	v_lshlrev_b32_e32 v54, 16, v80
	v_and_b32_e32 v55, 0xffff0000, v80
	v_lshlrev_b32_e32 v70, 16, v81
	v_and_b32_e32 v71, 0xffff0000, v81
	v_lshlrev_b32_e32 v50, 16, v74
	v_and_b32_e32 v51, 0xffff0000, v74
	v_lshlrev_b32_e32 v52, 16, v75
	v_and_b32_e32 v53, 0xffff0000, v75
	v_pk_mul_f32 v[70:71], v[56:57], v[70:71] op_sel_hi:[0,1]
	v_pk_mul_f32 v[54:55], v[56:57], v[54:55] op_sel_hi:[0,1]
	s_waitcnt vmcnt(3)
	v_lshlrev_b32_e32 v72, 16, v86
	v_and_b32_e32 v73, 0xffff0000, v86
	v_lshlrev_b32_e32 v74, 16, v87
	v_and_b32_e32 v75, 0xffff0000, v87
	v_pk_fma_f32 v[54:55], v[50:51], s[12:13], v[54:55] op_sel_hi:[1,0,1]
	v_pk_fma_f32 v[50:51], v[52:53], s[12:13], v[70:71] op_sel_hi:[1,0,1]
	v_pk_mul_f32 v[98:99], v[56:57], v[98:99] op_sel_hi:[0,1]
	v_pk_fma_f32 v[50:51], v[56:57], v[74:75], v[50:51] op_sel:[1,0,0]
	v_pk_fma_f32 v[52:53], v[56:57], v[72:73], v[54:55] op_sel:[1,0,0]
	s_waitcnt vmcnt(1)
	v_lshlrev_b32_e32 v72, 16, v90
	v_and_b32_e32 v73, 0xffff0000, v90
	v_lshlrev_b32_e32 v74, 16, v91
	v_and_b32_e32 v75, 0xffff0000, v91
	v_pk_fma_f32 v[34:35], v[34:35], s[12:13], v[98:99] op_sel_hi:[1,0,1]
	v_lshlrev_b32_e32 v54, 16, v88
	v_and_b32_e32 v55, 0xffff0000, v88
	v_lshlrev_b32_e32 v70, 16, v89
	v_and_b32_e32 v71, 0xffff0000, v89
	v_pk_mul_f32 v[74:75], v[56:57], v[74:75] op_sel_hi:[0,1]
	v_pk_mul_f32 v[72:73], v[56:57], v[72:73] op_sel_hi:[0,1]
	v_pk_fma_f32 v[34:35], v[56:57], v[100:101], v[34:35] op_sel:[1,0,0]
	s_waitcnt vmcnt(0)
	v_lshlrev_b32_e32 v76, 16, v92
	v_and_b32_e32 v77, 0xffff0000, v92
	v_lshlrev_b32_e32 v78, 16, v93
	v_and_b32_e32 v79, 0xffff0000, v93
	v_pk_fma_f32 v[72:73], v[54:55], s[12:13], v[72:73] op_sel_hi:[1,0,1]
	v_pk_fma_f32 v[54:55], v[70:71], s[12:13], v[74:75] op_sel_hi:[1,0,1]
	v_mov_b32_e32 v70, v36
	v_pk_fma_f32 v[54:55], v[56:57], v[78:79], v[54:55] op_sel:[1,0,0]
	v_pk_fma_f32 v[56:57], v[56:57], v[76:77], v[72:73] op_sel:[1,0,0]
	v_mov_b32_e32 v71, v34
	v_mov_b32_e32 v72, v37
	v_mov_b32_e32 v73, v35
	v_pk_add_f32 v[70:71], v[70:71], v[72:73]
	v_mov_b32_e32 v72, v32
	v_mov_b32_e32 v73, v30
	v_mov_b32_e32 v74, v33
	v_mov_b32_e32 v75, v31
	v_pk_add_f32 v[72:73], v[72:73], v[74:75]
	v_mov_b32_e32 v74, v28
	v_pk_add_f32 v[70:71], v[70:71], v[72:73]
	v_pk_mov_b32 v[72:73], v[28:29], v[26:27] op_sel:[1,0]
	v_mov_b32_e32 v75, v27
	v_pk_add_f32 v[72:73], v[72:73], v[74:75]
	v_add_f32_e32 v70, 0, v70
	v_pk_add_f32 v[72:73], v[72:73], v[72:73] op_sel:[0,1] op_sel_hi:[1,0]
	v_add_f32_e32 v70, v70, v71
	v_add_f32_e32 v74, v40, v41
	v_add_f32_e32 v76, v38, v39
	v_mov_b32_e32 v71, v44
	v_mov_b32_e32 v73, v45
	v_mov_b32_e32 v75, v42
	v_mov_b32_e32 v77, v43
	v_pk_add_f32 v[70:71], v[70:71], v[72:73]
	v_pk_add_f32 v[72:73], v[74:75], v[76:77]
	v_mov_b32_e32 v74, v48
	v_pk_add_f32 v[70:71], v[70:71], v[72:73]
	v_pk_mov_b32 v[72:73], v[48:49], v[46:47] op_sel:[1,0]
	v_mov_b32_e32 v75, v47
	v_pk_add_f32 v[72:73], v[72:73], v[74:75]
	v_pk_add_f32 v[70:71], v[70:71], v[70:71] op_sel:[0,1] op_sel_hi:[1,0]
	v_pk_add_f32 v[72:73], v[72:73], v[72:73] op_sel:[0,1] op_sel_hi:[1,0]
	v_add_f32_e32 v74, v52, v53
	v_add_f32_e32 v76, v50, v51
	v_mov_b32_e32 v71, v56
	v_mov_b32_e32 v73, v57
	v_mov_b32_e32 v75, v54
	v_mov_b32_e32 v77, v55
	v_pk_add_f32 v[70:71], v[70:71], v[72:73]
	v_pk_add_f32 v[72:73], v[74:75], v[76:77]
	s_nop 0
	v_pk_add_f32 v[70:71], v[70:71], v[72:73]
	s_nop 0
	v_add_f32_e32 v70, v70, v71
	v_cndmask_b32_e32 v71, v62, v64, vcc
	v_lshlrev_b32_e32 v78, 2, v71
	s_nop 1
	v_mov_b32_dpp v71, v70 quad_perm:[1,0,3,2] row_mask:0xf bank_mask:0xf
	v_cmp_lt_i32_e32 vcc, v65, v63
	s_waitcnt lgkmcnt(0)
	v_add_f32_e32 v70, v70, v71
	v_cndmask_b32_e32 v71, v62, v65, vcc
	v_lshlrev_b32_e32 v86, 2, v71
	s_nop 1
	v_mov_b32_dpp v71, v70 quad_perm:[2,3,0,1] row_mask:0xf bank_mask:0xf
	v_cmp_lt_i32_e32 vcc, v66, v63
	s_waitcnt lgkmcnt(0)
	v_add_f32_e32 v70, v70, v71
	v_cndmask_b32_e32 v71, v62, v66, vcc
	v_lshlrev_b32_e32 v102, 2, v71
	s_nop 1
	v_mov_b32_dpp v71, v70 row_half_mirror row_mask:0xf bank_mask:0xf
	v_cmp_lt_i32_e32 vcc, v67, v63
	s_waitcnt lgkmcnt(0)
	v_add_f32_e32 v70, v70, v71
	v_cndmask_b32_e32 v71, v62, v67, vcc
	v_lshlrev_b32_e32 v118, 2, v71
	s_nop 1
	v_mov_b32_dpp v71, v70 row_mirror row_mask:0xf bank_mask:0xf
	v_cmp_lt_i32_e32 vcc, v68, v63
	s_waitcnt lgkmcnt(0)
	v_add_f32_e32 v70, v70, v71
	v_cndmask_b32_e32 v71, v62, v68, vcc
	v_lshlrev_b32_e32 v134, 2, v71
	v_mov_b32_e32 v71, v70
	s_nop 1
	v_permlane16_swap_b32_e32 v71, v70
	v_cmp_lt_i32_e32 vcc, v69, v63
	s_waitcnt lgkmcnt(0)
	v_add_f32_e32 v70, v70, v71
	v_cndmask_b32_e32 v71, v62, v69, vcc
	v_lshlrev_b32_e32 v135, 2, v71
	v_mov_b32_e32 v71, v70
	s_nop 1
	v_permlane32_swap_b32_e32 v71, v70
	s_waitcnt lgkmcnt(0)
	v_add_f32_e32 v79, v70, v71
	v_fmamk_f32 v37, v79, 0xba000000, v37
	v_fmamk_f32 v35, v79, 0xba000000, v35
	v_fmamk_f32 v33, v79, 0xba000000, v33
	v_fmac_f32_e32 v36, 0xba000000, v79
	v_fmamk_f32 v31, v79, 0xba000000, v31
	v_fmac_f32_e32 v34, 0xba000000, v79
	v_mov_b32_e32 v72, v37
	v_mov_b32_e32 v73, v35
	v_fmac_f32_e32 v32, 0xba000000, v79
	v_fmac_f32_e32 v30, 0xba000000, v79
	v_mov_b32_e32 v70, v36
	v_mov_b32_e32 v71, v34
	v_pk_mul_f32 v[72:73], v[72:73], v[72:73]
	v_mov_b32_e32 v74, v33
	v_mov_b32_e32 v75, v31
	v_pk_fma_f32 v[70:71], v[70:71], v[70:71], v[72:73]
	v_mov_b32_e32 v72, v32
	v_mov_b32_e32 v73, v30
	v_pk_mul_f32 v[74:75], v[74:75], v[74:75]
	v_fmamk_f32 v29, v79, 0xba000000, v29
	v_pk_fma_f32 v[72:73], v[72:73], v[72:73], v[74:75]
	v_fmac_f32_e32 v28, 0xba000000, v79
	v_pk_add_f32 v[70:71], v[70:71], v[72:73]
	v_fmamk_f32 v27, v79, 0xba000000, v27
	v_fmac_f32_e32 v26, 0xba000000, v79
	v_pk_add_f32 v[70:71], v[70:71], v[70:71] op_sel_hi:[0,1]
	v_pk_mul_f32 v[72:73], v[26:27], v[26:27]
	v_pk_mul_f32 v[74:75], v[28:29], v[28:29]
	v_fmac_f32_e32 v40, 0xba000000, v79
	v_pk_mov_b32 v[76:77], v[74:75], v[72:73] op_sel:[1,0]
	v_mov_b32_e32 v75, v73
	v_fmamk_f32 v41, v79, 0xba000000, v41
	v_fmac_f32_e32 v38, 0xba000000, v79
	v_mul_f32_e32 v70, v40, v40
	v_pk_add_f32 v[72:73], v[76:77], v[74:75]
	v_fmamk_f32 v39, v79, 0xba000000, v39
	v_pk_fma_f32 v[74:75], v[40:41], v[40:41], v[70:71] op_sel_hi:[1,1,0]
	v_mul_f32_e32 v70, v38, v38
	v_pk_add_f32 v[72:73], v[72:73], v[72:73] op_sel_hi:[0,1]
	v_pk_fma_f32 v[76:77], v[38:39], v[38:39], v[70:71] op_sel_hi:[1,1,0]
	v_fmamk_f32 v43, v79, 0xba000000, v43
	v_fmac_f32_e32 v42, 0xba000000, v79
	v_fmamk_f32 v45, v79, 0xba000000, v45
	v_fmac_f32_e32 v44, 0xba000000, v79
	v_mul_f32_e32 v74, v44, v44
	v_mul_f32_e32 v76, v45, v45
	v_mul_f32_e32 v72, v42, v42
	v_mul_f32_e32 v70, v43, v43
	v_pk_add_f32 v[74:75], v[74:75], v[76:77]
	v_pk_add_f32 v[70:71], v[72:73], v[70:71]
	v_fmamk_f32 v49, v79, 0xba000000, v49
	v_pk_add_f32 v[70:71], v[74:75], v[70:71]
	v_fmac_f32_e32 v48, 0xba000000, v79
	v_fmamk_f32 v47, v79, 0xba000000, v47
	v_fmac_f32_e32 v46, 0xba000000, v79
	v_pk_add_f32 v[70:71], v[70:71], v[70:71] op_sel_hi:[0,1]
	v_pk_mul_f32 v[72:73], v[46:47], v[46:47]
	v_pk_mul_f32 v[74:75], v[48:49], v[48:49]
	v_fmac_f32_e32 v52, 0xba000000, v79
	v_pk_mov_b32 v[76:77], v[74:75], v[72:73] op_sel:[1,0]
	v_mov_b32_e32 v75, v73
	v_fmamk_f32 v53, v79, 0xba000000, v53
	v_fmac_f32_e32 v50, 0xba000000, v79
	v_mul_f32_e32 v70, v52, v52
	v_pk_add_f32 v[72:73], v[76:77], v[74:75]
	v_fmamk_f32 v51, v79, 0xba000000, v51
	v_pk_fma_f32 v[74:75], v[52:53], v[52:53], v[70:71] op_sel_hi:[1,1,0]
	v_mul_f32_e32 v70, v50, v50
	v_pk_add_f32 v[72:73], v[72:73], v[72:73] op_sel_hi:[0,1]
	v_pk_fma_f32 v[76:77], v[50:51], v[50:51], v[70:71] op_sel_hi:[1,1,0]
	v_fmamk_f32 v55, v79, 0xba000000, v55
	v_fmac_f32_e32 v54, 0xba000000, v79
	v_fmamk_f32 v57, v79, 0xba000000, v57
	v_fmac_f32_e32 v56, 0xba000000, v79
	v_mul_f32_e32 v74, v56, v56
	v_mul_f32_e32 v76, v57, v57
	v_mul_f32_e32 v72, v54, v54
	v_mul_f32_e32 v70, v55, v55
	v_pk_add_f32 v[74:75], v[74:75], v[76:77]
	v_pk_add_f32 v[70:71], v[72:73], v[70:71]
	s_nop 0
	v_pk_add_f32 v[70:71], v[74:75], v[70:71]
	s_nop 0
	v_add_f32_e32 v79, v70, v71
	s_nop 1
	v_mov_b32_dpp v78, v79 quad_perm:[1,0,3,2] row_mask:0xf bank_mask:0xf
	global_load_dwordx4 v[70:73], v[2:3], off
	global_load_dwordx4 v[74:77], v[4:5], off
	s_waitcnt lgkmcnt(0)
	v_add_f32_e32 v94, v79, v78
	s_nop 1
	v_mov_b32_dpp v95, v94 quad_perm:[2,3,0,1] row_mask:0xf bank_mask:0xf
	global_load_dwordx4 v[78:81], v[2:3], off offset:1024
	global_load_dwordx4 v[82:85], v[4:5], off offset:1024
	global_load_dwordx4 v[86:89], v[2:3], off offset:2048
	global_load_dwordx4 v[90:93], v[4:5], off offset:2048
	s_waitcnt lgkmcnt(0)
	v_add_f32_e32 v110, v94, v95
	s_nop 1
	v_mov_b32_dpp v111, v110 row_half_mirror row_mask:0xf bank_mask:0xf
	global_load_dwordx4 v[94:97], v[2:3], off offset:3072
	global_load_dwordx4 v[98:101], v[4:5], off offset:3072
	global_load_dwordx4 v[102:105], v[6:7], off
	global_load_dwordx4 v[106:109], v[8:9], off
	s_waitcnt lgkmcnt(0)
	v_add_f32_e32 v126, v110, v111
	s_nop 1
	v_mov_b32_dpp v127, v126 row_mirror row_mask:0xf bank_mask:0xf
	global_load_dwordx4 v[110:113], v[10:11], off
	global_load_dwordx4 v[114:117], v[12:13], off
	global_load_dwordx4 v[118:121], v[14:15], off
	global_load_dwordx4 v[122:125], v[16:17], off
	s_waitcnt lgkmcnt(0)
	v_add_f32_e32 v136, v126, v127
	global_load_dwordx4 v[126:129], v[18:19], off
	global_load_dwordx4 v[130:133], v[20:21], off
	v_mov_b32_e32 v134, v136
	s_nop 1
	v_permlane16_swap_b32_e32 v134, v136
	s_waitcnt lgkmcnt(0)
	v_add_f32_e32 v134, v136, v134
	v_mov_b32_e32 v135, v134
	s_nop 1
	v_permlane32_swap_b32_e32 v135, v134
	s_waitcnt lgkmcnt(0)
	v_add_f32_e32 v134, v134, v135
	v_fmamk_f32 v134, v134, 0x3a000000, v59
	v_mul_f32_e32 v135, 0x4f800000, v134
	v_cmp_gt_f32_e32 vcc, s29, v134
	s_nop 1
	v_cndmask_b32_e32 v134, v134, v135, vcc
	v_sqrt_f32_e32 v135, v134
	s_nop 0
	v_add_u32_e32 v136, -1, v135
	v_fma_f32 v137, -v136, v135, v134
	v_cmp_ge_f32_e64 s[2:3], 0, v137
	v_add_u32_e32 v137, 1, v135
	s_nop 0
	v_cndmask_b32_e64 v136, v135, v136, s[2:3]
	v_fma_f32 v135, -v137, v135, v134
	v_cmp_lt_f32_e64 s[2:3], 0, v135
	s_nop 1
	v_cndmask_b32_e64 v135, v136, v137, s[2:3]
	v_mul_f32_e32 v136, 0x37800000, v135
	v_cndmask_b32_e32 v135, v135, v136, vcc
	v_cmp_class_f32_e32 vcc, v134, v60
	s_nop 1
	v_cndmask_b32_e32 v134, v135, v134, vcc
	v_div_scale_f32 v135, s[2:3], v134, v134, 1.0
	v_rcp_f32_e32 v136, v135
	s_lshl_b64 s[2:3], s[14:15], 13
	s_add_u32 s2, s64, s2
	s_addc_u32 s3, s65, s3
	v_fma_f32 v137, -v135, v136, 1.0
	v_fmac_f32_e32 v136, v137, v136
	v_div_scale_f32 v137, vcc, 1.0, v134, 1.0
	v_mul_f32_e32 v138, v137, v136
	v_fma_f32 v139, -v135, v138, v137
	v_fmac_f32_e32 v138, v139, v136
	v_fma_f32 v135, -v135, v138, v137
	v_div_fmas_f32 v135, v135, v136, v138
	v_div_fixup_f32 v134, v135, v134, 1.0
	v_pk_mul_f32 v[32:33], v[32:33], v[134:135] op_sel_hi:[1,0]
	v_pk_mul_f32 v[34:35], v[34:35], v[134:135] op_sel_hi:[1,0]
	v_pk_mul_f32 v[30:31], v[30:31], v[134:135] op_sel_hi:[1,0]
	v_pk_mul_f32 v[36:37], v[36:37], v[134:135] op_sel_hi:[1,0]
	s_waitcnt vmcnt(14)
	v_pk_fma_f32 v[72:73], v[72:73], v[32:33], v[76:77]
	v_pk_mul_f32 v[26:27], v[26:27], v[134:135] op_sel_hi:[1,0]
	v_pk_fma_f32 v[70:71], v[70:71], v[36:37], v[74:75]
	s_waitcnt vmcnt(12)
	v_pk_fma_f32 v[32:33], v[80:81], v[30:31], v[84:85]
	v_pk_fma_f32 v[30:31], v[78:79], v[34:35], v[82:83]
	v_pk_mul_f32 v[34:35], v[28:29], v[134:135] op_sel_hi:[1,0]
	s_waitcnt vmcnt(10)
	v_pk_fma_f32 v[28:29], v[88:89], v[26:27], v[92:93]
	v_pk_fma_f32 v[26:27], v[86:87], v[34:35], v[90:91]
	v_pk_mul_f32 v[34:35], v[40:41], v[134:135] op_sel_hi:[1,0]
	v_pk_mul_f32 v[36:37], v[38:39], v[134:135] op_sel_hi:[1,0]
	v_pk_mul_f32 v[38:39], v[44:45], v[134:135] op_sel_hi:[1,0]
	v_pk_mul_f32 v[44:45], v[46:47], v[134:135] op_sel_hi:[1,0]
	v_pk_mul_f32 v[46:47], v[52:53], v[134:135] op_sel_hi:[1,0]
	v_pk_mul_f32 v[52:53], v[54:55], v[134:135] op_sel_hi:[1,0]
	v_lshl_add_u64 v[54:55], v[0:1], 2, s[2:3]
	s_waitcnt vmcnt(8)
	v_pk_fma_f32 v[36:37], v[96:97], v[36:37], v[100:101]
	v_pk_fma_f32 v[34:35], v[94:95], v[34:35], v[98:99]
	v_pk_mul_f32 v[40:41], v[42:43], v[134:135] op_sel_hi:[1,0]
	global_store_dwordx4 v[54:55], v[70:73], off
	global_store_dwordx4 v[54:55], v[30:33], off offset:1024
	global_store_dwordx4 v[54:55], v[26:29], off offset:2048
	global_store_dwordx4 v[54:55], v[34:37], off offset:3072
	s_waitcnt vmcnt(10)
	v_pk_fma_f32 v[40:41], v[104:105], v[40:41], v[108:109]
	v_add_co_u32_e32 v26, vcc, s30, v54
	v_pk_fma_f32 v[38:39], v[102:103], v[38:39], v[106:107]
	v_pk_mul_f32 v[42:43], v[48:49], v[134:135] op_sel_hi:[1,0]
	v_pk_mul_f32 v[48:49], v[50:51], v[134:135] op_sel_hi:[1,0]
	v_pk_mul_f32 v[50:51], v[56:57], v[134:135] op_sel_hi:[1,0]
	v_addc_co_u32_e32 v27, vcc, 0, v55, vcc
	s_waitcnt vmcnt(8)
	v_pk_fma_f32 v[44:45], v[112:113], v[44:45], v[116:117]
	v_pk_fma_f32 v[42:43], v[110:111], v[42:43], v[114:115]
	s_waitcnt vmcnt(6)
	v_pk_fma_f32 v[48:49], v[120:121], v[48:49], v[124:125]
	v_pk_fma_f32 v[46:47], v[118:119], v[46:47], v[122:123]
	s_waitcnt vmcnt(4)
	v_pk_fma_f32 v[52:53], v[128:129], v[52:53], v[132:133]
	v_pk_fma_f32 v[50:51], v[126:127], v[50:51], v[130:131]
	global_store_dwordx4 v[26:27], v[38:41], off
	global_store_dwordx4 v[26:27], v[42:45], off offset:1024
	global_store_dwordx4 v[26:27], v[46:49], off offset:2048
	global_store_dwordx4 v[26:27], v[50:53], off offset:3072
	s_and_saveexec_b64 s[2:3], s[0:1]
	s_cbranch_execz .LBB0_1991
	s_lshl_b64 s[14:15], s[14:15], 2
	s_add_u32 s14, s22, s14
	s_addc_u32 s15, s23, s15
	global_store_dword v58, v61, s[14:15]
	s_branch .LBB0_1991

.LBB0_2073:
	s_abs_i32 s1, s15
	s_mul_hi_u32 s4, s1, s20
	s_mul_i32 s4, s4, s19
	s_sub_i32 s1, s1, s4
	s_ashr_i32 s0, s15, 31
	s_sub_i32 s4, s1, s19
	s_cmp_ge_u32 s1, s19
	s_cselect_b32 s1, s4, s1
	s_sub_i32 s4, s1, s19
	s_cmp_ge_u32 s1, s19
	s_cselect_b32 s1, s4, s1
	s_xor_b32 s1, s1, s0
	s_sub_i32 s0, s1, s0
	s_add_i32 s4, s18, s0
	s_cmpk_gt_i32 s4, 0x3fff
	s_cbranch_scc1 .LBB0_2072
	s_lshl_b32 s0, s4, 1
	s_ashr_i32 s1, s0, 31
	s_lshl_b64 s[0:1], s[0:1], 2
	s_add_u32 s6, s11, s0
	s_addc_u32 s7, s12, s1
	s_ashr_i32 s5, s4, 31
	s_lshl_b64 s[8:9], s[4:5], 2
	s_add_u32 s8, s13, s8
	s_addc_u32 s9, s14, s9
	global_load_dwordx2 v[26:27], v58, s[6:7]
	global_load_dword v28, v58, s[8:9]
	s_waitcnt vmcnt(1)
	v_readfirstlane_b32 s8, v26
	s_waitcnt vmcnt(0)
	v_readfirstlane_b32 s6, v28
	s_cmp_lg_u32 s6, 0
	v_readfirstlane_b32 s6, v27
	s_cbranch_scc1 .LBB0_2072
	s_add_u32 s0, s3, s0
	s_addc_u32 s1, s10, s1
	s_lshl_b64 s[22:23], s[4:5], 12
	v_lshl_add_u64 v[28:29], v[22:23], 0, s[22:23]
	global_load_dwordx2 v[26:27], v[28:29], off
	global_load_dwordx2 v[30:31], v[28:29], off offset:512
	global_load_dwordx2 v[32:33], v[28:29], off offset:1024
	s_ashr_i32 s9, s8, 31
	s_ashr_i32 s7, s6, 31
	s_lshl_b64 s[8:9], s[8:9], 12
	s_lshl_b64 s[6:7], s[6:7], 12
	v_lshl_add_u64 v[34:35], v[24:25], 0, s[8:9]
	v_lshl_add_u64 v[38:39], v[24:25], 0, s[6:7]
	global_load_dwordx2 v[36:37], v[34:35], off
	global_load_dwordx2 v[40:41], v[38:39], off
	global_load_dwordx2 v[42:43], v[34:35], off offset:512
	global_load_dwordx2 v[44:45], v[38:39], off offset:512
	global_load_dwordx2 v[46:47], v[34:35], off offset:1024
	global_load_dwordx2 v[48:49], v[38:39], off offset:1024
	global_load_dwordx2 v[56:57], v58, s[0:1]
	global_load_dwordx2 v[50:51], v[28:29], off offset:1536
	global_load_dwordx2 v[52:53], v[34:35], off offset:1536
	global_load_dwordx2 v[54:55], v[38:39], off offset:1536
	global_load_dwordx2 v[70:71], v[28:29], off offset:2048
	global_load_dwordx2 v[72:73], v[28:29], off offset:2560
	global_load_dwordx2 v[74:75], v[28:29], off offset:3072
	global_load_dwordx2 v[76:77], v[34:35], off offset:2048
	global_load_dwordx2 v[78:79], v[34:35], off offset:2560
	global_load_dwordx2 v[80:81], v[34:35], off offset:3072
	global_load_dwordx2 v[82:83], v[38:39], off offset:2048
	global_load_dwordx2 v[84:85], v[38:39], off offset:2560
	global_load_dwordx2 v[86:87], v[38:39], off offset:3072
	global_load_dwordx2 v[88:89], v[28:29], off offset:3584
	global_load_dwordx2 v[90:91], v[34:35], off offset:3584
	v_cmp_lt_i32_e32 vcc, v63, v62
	s_waitcnt vmcnt(19)
	v_lshlrev_b32_e32 v96, 16, v40
	s_waitcnt vmcnt(18)
	v_lshlrev_b32_e32 v98, 16, v42
	v_and_b32_e32 v99, 0xffff0000, v42
	v_lshlrev_b32_e32 v42, 16, v43
	v_and_b32_e32 v43, 0xffff0000, v43
	s_waitcnt vmcnt(16)
	v_lshlrev_b32_e32 v102, 16, v46
	v_and_b32_e32 v103, 0xffff0000, v46
	s_waitcnt vmcnt(14)
	v_pk_mul_f32 v[42:43], v[56:57], v[42:43] op_sel_hi:[0,1]
	v_pk_mul_f32 v[102:103], v[56:57], v[102:103] op_sel_hi:[0,1]
	v_and_b32_e32 v97, 0xffff0000, v40
	v_lshlrev_b32_e32 v28, 16, v26
	v_lshlrev_b32_e32 v34, 16, v30
	v_and_b32_e32 v35, 0xffff0000, v30
	v_lshlrev_b32_e32 v30, 16, v31
	v_and_b32_e32 v31, 0xffff0000, v31
	v_lshlrev_b32_e32 v92, 16, v32
	v_and_b32_e32 v93, 0xffff0000, v32
	v_pk_fma_f32 v[30:31], v[30:31], s[2:3], v[42:43] op_sel_hi:[1,0,1]
	v_pk_fma_f32 v[42:43], v[92:93], s[2:3], v[102:103] op_sel_hi:[1,0,1]
	global_load_dwordx2 v[92:93], v[38:39], off offset:3584
	v_lshlrev_b32_e32 v94, 16, v36
	v_and_b32_e32 v95, 0xffff0000, v36
	v_and_b32_e32 v29, 0xffff0000, v26
	v_lshlrev_b32_e32 v36, 16, v37
	v_and_b32_e32 v37, 0xffff0000, v37
	v_pk_mul_f32 v[94:95], v[56:57], v[94:95] op_sel_hi:[0,1]
	v_lshlrev_b32_e32 v26, 16, v27
	v_and_b32_e32 v27, 0xffff0000, v27
	v_lshlrev_b32_e32 v100, 16, v44
	v_and_b32_e32 v101, 0xffff0000, v44
	v_lshlrev_b32_e32 v44, 16, v45
	v_and_b32_e32 v45, 0xffff0000, v45
	v_lshlrev_b32_e32 v46, 16, v47
	v_and_b32_e32 v47, 0xffff0000, v47
	v_lshlrev_b32_e32 v104, 16, v48
	v_and_b32_e32 v105, 0xffff0000, v48
	v_pk_mul_f32 v[36:37], v[56:57], v[36:37] op_sel_hi:[0,1]
	v_pk_fma_f32 v[28:29], v[28:29], s[2:3], v[94:95] op_sel_hi:[1,0,1]
	v_lshlrev_b32_e32 v32, 16, v33
	v_and_b32_e32 v33, 0xffff0000, v33
	v_lshlrev_b32_e32 v40, 16, v41
	v_and_b32_e32 v41, 0xffff0000, v41
	v_pk_mul_f32 v[46:47], v[56:57], v[46:47] op_sel_hi:[0,1]
	v_pk_fma_f32 v[26:27], v[26:27], s[2:3], v[36:37] op_sel_hi:[1,0,1]
	v_pk_fma_f32 v[36:37], v[56:57], v[96:97], v[28:29] op_sel:[1,0,0]
	v_pk_fma_f32 v[30:31], v[56:57], v[44:45], v[30:31] op_sel:[1,0,0]
	v_pk_fma_f32 v[28:29], v[56:57], v[104:105], v[42:43] op_sel:[1,0,0]
	s_waitcnt vmcnt(13)
	v_lshlrev_b32_e32 v42, 16, v52
	v_and_b32_e32 v43, 0xffff0000, v52
	v_lshlrev_b32_e32 v44, 16, v53
	v_and_b32_e32 v45, 0xffff0000, v53
	v_lshlrev_b32_e32 v48, 16, v49
	v_and_b32_e32 v49, 0xffff0000, v49
	v_pk_fma_f32 v[46:47], v[32:33], s[2:3], v[46:47] op_sel_hi:[1,0,1]
	v_pk_fma_f32 v[32:33], v[56:57], v[40:41], v[26:27] op_sel:[1,0,0]
	v_lshlrev_b32_e32 v40, 16, v50
	v_and_b32_e32 v41, 0xffff0000, v50
	v_lshlrev_b32_e32 v38, 16, v51
	v_and_b32_e32 v39, 0xffff0000, v51
	v_pk_mul_f32 v[44:45], v[56:57], v[44:45] op_sel_hi:[0,1]
	v_pk_mul_f32 v[42:43], v[56:57], v[42:43] op_sel_hi:[0,1]
	v_pk_fma_f32 v[26:27], v[56:57], v[48:49], v[46:47] op_sel:[1,0,0]
	s_waitcnt vmcnt(12)
	v_lshlrev_b32_e32 v46, 16, v54
	v_and_b32_e32 v47, 0xffff0000, v54
	v_lshlrev_b32_e32 v48, 16, v55
	v_and_b32_e32 v49, 0xffff0000, v55
	v_pk_fma_f32 v[40:41], v[40:41], s[2:3], v[42:43] op_sel_hi:[1,0,1]
	v_pk_fma_f32 v[38:39], v[38:39], s[2:3], v[44:45] op_sel_hi:[1,0,1]
	v_pk_fma_f32 v[40:41], v[56:57], v[46:47], v[40:41] op_sel:[1,0,0]
	v_pk_fma_f32 v[38:39], v[56:57], v[48:49], v[38:39] op_sel:[1,0,0]
	s_waitcnt vmcnt(8)
	v_lshlrev_b32_e32 v46, 16, v76
	v_and_b32_e32 v47, 0xffff0000, v76
	v_lshlrev_b32_e32 v48, 16, v77
	v_and_b32_e32 v49, 0xffff0000, v77
	v_lshlrev_b32_e32 v42, 16, v70
	v_and_b32_e32 v43, 0xffff0000, v70
	v_lshlrev_b32_e32 v44, 16, v71
	v_and_b32_e32 v45, 0xffff0000, v71
	v_pk_mul_f32 v[48:49], v[56:57], v[48:49] op_sel_hi:[0,1]
	v_pk_mul_f32 v[46:47], v[56:57], v[46:47] op_sel_hi:[0,1]
	s_waitcnt vmcnt(5)
	v_lshlrev_b32_e32 v50, 16, v82
	v_and_b32_e32 v51, 0xffff0000, v82
	v_lshlrev_b32_e32 v52, 16, v83
	v_and_b32_e32 v53, 0xffff0000, v83
	v_pk_fma_f32 v[46:47], v[42:43], s[2:3], v[46:47] op_sel_hi:[1,0,1]
	v_pk_fma_f32 v[42:43], v[44:45], s[2:3], v[48:49] op_sel_hi:[1,0,1]
	v_pk_fma_f32 v[44:45], v[56:57], v[50:51], v[46:47] op_sel:[1,0,0]
	v_pk_fma_f32 v[42:43], v[56:57], v[52:53], v[42:43] op_sel:[1,0,0]
	v_lshlrev_b32_e32 v50, 16, v78
	v_and_b32_e32 v51, 0xffff0000, v78
	v_lshlrev_b32_e32 v52, 16, v79
	v_and_b32_e32 v53, 0xffff0000, v79
	v_lshlrev_b32_e32 v46, 16, v72
	v_and_b32_e32 v47, 0xffff0000, v72
	v_lshlrev_b32_e32 v48, 16, v73
	v_and_b32_e32 v49, 0xffff0000, v73
	v_pk_mul_f32 v[52:53], v[56:57], v[52:53] op_sel_hi:[0,1]
	v_pk_mul_f32 v[50:51], v[56:57], v[50:51] op_sel_hi:[0,1]
	s_waitcnt vmcnt(4)
	v_lshlrev_b32_e32 v54, 16, v84
	v_and_b32_e32 v55, 0xffff0000, v84
	v_lshlrev_b32_e32 v70, 16, v85
	v_and_b32_e32 v71, 0xffff0000, v85
	v_pk_fma_f32 v[50:51], v[46:47], s[2:3], v[50:51] op_sel_hi:[1,0,1]
	v_pk_fma_f32 v[46:47], v[48:49], s[2:3], v[52:53] op_sel_hi:[1,0,1]
	v_pk_fma_f32 v[48:49], v[56:57], v[54:55], v[50:51] op_sel:[1,0,0]
	v_pk_fma_f32 v[46:47], v[56:57], v[70:71], v[46:47] op_sel:[1,0,0]
	v_lshlrev_b32_e32 v54, 16, v80
	v_and_b32_e32 v55, 0xffff0000, v80
	v_lshlrev_b32_e32 v70, 16, v81
	v_and_b32_e32 v71, 0xffff0000, v81
	v_lshlrev_b32_e32 v50, 16, v74
	v_and_b32_e32 v51, 0xffff0000, v74
	v_lshlrev_b32_e32 v52, 16, v75
	v_and_b32_e32 v53, 0xffff0000, v75
	v_pk_mul_f32 v[70:71], v[56:57], v[70:71] op_sel_hi:[0,1]
	v_pk_mul_f32 v[54:55], v[56:57], v[54:55] op_sel_hi:[0,1]
	s_waitcnt vmcnt(3)
	v_lshlrev_b32_e32 v72, 16, v86
	v_and_b32_e32 v73, 0xffff0000, v86
	v_lshlrev_b32_e32 v74, 16, v87
	v_and_b32_e32 v75, 0xffff0000, v87
	v_pk_fma_f32 v[54:55], v[50:51], s[2:3], v[54:55] op_sel_hi:[1,0,1]
	v_pk_fma_f32 v[50:51], v[52:53], s[2:3], v[70:71] op_sel_hi:[1,0,1]
	v_pk_mul_f32 v[98:99], v[56:57], v[98:99] op_sel_hi:[0,1]
	v_pk_fma_f32 v[50:51], v[56:57], v[74:75], v[50:51] op_sel:[1,0,0]
	v_pk_fma_f32 v[52:53], v[56:57], v[72:73], v[54:55] op_sel:[1,0,0]
	s_waitcnt vmcnt(1)
	v_lshlrev_b32_e32 v72, 16, v90
	v_and_b32_e32 v73, 0xffff0000, v90
	v_lshlrev_b32_e32 v74, 16, v91
	v_and_b32_e32 v75, 0xffff0000, v91
	v_pk_fma_f32 v[34:35], v[34:35], s[2:3], v[98:99] op_sel_hi:[1,0,1]
	v_lshlrev_b32_e32 v54, 16, v88
	v_and_b32_e32 v55, 0xffff0000, v88
	v_lshlrev_b32_e32 v70, 16, v89
	v_and_b32_e32 v71, 0xffff0000, v89
	v_pk_mul_f32 v[74:75], v[56:57], v[74:75] op_sel_hi:[0,1]
	v_pk_mul_f32 v[72:73], v[56:57], v[72:73] op_sel_hi:[0,1]
	v_pk_fma_f32 v[34:35], v[56:57], v[100:101], v[34:35] op_sel:[1,0,0]
	s_waitcnt vmcnt(0)
	v_lshlrev_b32_e32 v76, 16, v92
	v_and_b32_e32 v77, 0xffff0000, v92
	v_lshlrev_b32_e32 v78, 16, v93
	v_and_b32_e32 v79, 0xffff0000, v93
	v_pk_fma_f32 v[72:73], v[54:55], s[2:3], v[72:73] op_sel_hi:[1,0,1]
	v_pk_fma_f32 v[54:55], v[70:71], s[2:3], v[74:75] op_sel_hi:[1,0,1]
	v_mov_b32_e32 v70, v36
	v_pk_fma_f32 v[54:55], v[56:57], v[78:79], v[54:55] op_sel:[1,0,0]
	v_pk_fma_f32 v[56:57], v[56:57], v[76:77], v[72:73] op_sel:[1,0,0]
	v_mov_b32_e32 v71, v34
	v_mov_b32_e32 v72, v37
	v_mov_b32_e32 v73, v35
	v_pk_add_f32 v[70:71], v[70:71], v[72:73]
	v_mov_b32_e32 v72, v32
	v_mov_b32_e32 v73, v30
	v_mov_b32_e32 v74, v33
	v_mov_b32_e32 v75, v31
	v_pk_add_f32 v[72:73], v[72:73], v[74:75]
	v_mov_b32_e32 v74, v28
	v_pk_add_f32 v[70:71], v[70:71], v[72:73]
	v_pk_mov_b32 v[72:73], v[28:29], v[26:27] op_sel:[1,0]
	v_mov_b32_e32 v75, v27
	v_pk_add_f32 v[72:73], v[72:73], v[74:75]
	v_add_f32_e32 v69, 0, v70
	v_pk_add_f32 v[72:73], v[72:73], v[72:73] op_sel:[0,1] op_sel_hi:[1,0]
	v_add_f32_e32 v70, v69, v71
	v_add_f32_e32 v74, v40, v41
	v_add_f32_e32 v76, v38, v39
	v_mov_b32_e32 v71, v44
	v_mov_b32_e32 v73, v45
	v_mov_b32_e32 v75, v42
	v_mov_b32_e32 v77, v43
	v_pk_add_f32 v[70:71], v[70:71], v[72:73]
	v_pk_add_f32 v[72:73], v[74:75], v[76:77]
	v_mov_b32_e32 v74, v48
	v_pk_add_f32 v[70:71], v[70:71], v[72:73]
	v_pk_mov_b32 v[72:73], v[48:49], v[46:47] op_sel:[1,0]
	v_mov_b32_e32 v75, v47
	v_pk_add_f32 v[72:73], v[72:73], v[74:75]
	v_pk_add_f32 v[70:71], v[70:71], v[70:71] op_sel:[0,1] op_sel_hi:[1,0]
	v_pk_add_f32 v[72:73], v[72:73], v[72:73] op_sel:[0,1] op_sel_hi:[1,0]
	v_add_f32_e32 v74, v52, v53
	v_add_f32_e32 v76, v50, v51
	v_mov_b32_e32 v71, v56
	v_mov_b32_e32 v73, v57
	v_mov_b32_e32 v75, v54
	v_mov_b32_e32 v77, v55
	v_pk_add_f32 v[70:71], v[70:71], v[72:73]
	v_pk_add_f32 v[72:73], v[74:75], v[76:77]
	s_nop 0
	v_pk_add_f32 v[70:71], v[70:71], v[72:73]
	s_nop 0
	v_add_f32_e32 v69, v70, v71
	v_cndmask_b32_e32 v70, v61, v63, vcc
	v_lshlrev_b32_e32 v78, 2, v70
	s_nop 1
	v_mov_b32_dpp v70, v69 quad_perm:[1,0,3,2] row_mask:0xf bank_mask:0xf
	v_cmp_lt_i32_e32 vcc, v64, v62
	s_waitcnt lgkmcnt(0)
	v_add_f32_e32 v69, v69, v70
	v_cndmask_b32_e32 v70, v61, v64, vcc
	v_lshlrev_b32_e32 v86, 2, v70
	s_nop 1
	v_mov_b32_dpp v70, v69 quad_perm:[2,3,0,1] row_mask:0xf bank_mask:0xf
	v_cmp_lt_i32_e32 vcc, v65, v62
	s_waitcnt lgkmcnt(0)
	v_add_f32_e32 v69, v69, v70
	v_cndmask_b32_e32 v70, v61, v65, vcc
	v_lshlrev_b32_e32 v102, 2, v70
	s_nop 1
	v_mov_b32_dpp v70, v69 row_half_mirror row_mask:0xf bank_mask:0xf
	v_cmp_lt_i32_e32 vcc, v66, v62
	s_waitcnt lgkmcnt(0)
	v_add_f32_e32 v69, v69, v70
	v_cndmask_b32_e32 v70, v61, v66, vcc
	v_lshlrev_b32_e32 v118, 2, v70
	s_nop 1
	v_mov_b32_dpp v70, v69 row_mirror row_mask:0xf bank_mask:0xf
	v_cmp_lt_i32_e32 vcc, v67, v62
	s_waitcnt lgkmcnt(0)
	v_add_f32_e32 v69, v69, v70
	v_cndmask_b32_e32 v70, v61, v67, vcc
	v_lshlrev_b32_e32 v134, 2, v70
	v_mov_b32_e32 v70, v69
	s_nop 1
	v_permlane16_swap_b32_e32 v70, v69
	v_cmp_lt_i32_e32 vcc, v68, v62
	s_waitcnt lgkmcnt(0)
	v_add_f32_e32 v69, v69, v70
	v_cndmask_b32_e32 v70, v61, v68, vcc
	v_lshlrev_b32_e32 v135, 2, v70
	v_mov_b32_e32 v70, v69
	s_nop 1
	v_permlane32_swap_b32_e32 v70, v69
	s_waitcnt lgkmcnt(0)
	v_add_f32_e32 v69, v69, v70
	v_fmamk_f32 v37, v69, 0xba000000, v37
	v_fmamk_f32 v35, v69, 0xba000000, v35
	v_fmamk_f32 v33, v69, 0xba000000, v33
	v_fmac_f32_e32 v36, 0xba000000, v69
	v_fmamk_f32 v31, v69, 0xba000000, v31
	v_fmac_f32_e32 v34, 0xba000000, v69
	v_mov_b32_e32 v72, v37
	v_mov_b32_e32 v73, v35
	v_fmac_f32_e32 v32, 0xba000000, v69
	v_fmac_f32_e32 v30, 0xba000000, v69
	v_mov_b32_e32 v70, v36
	v_mov_b32_e32 v71, v34
	v_pk_mul_f32 v[72:73], v[72:73], v[72:73]
	v_mov_b32_e32 v74, v33
	v_mov_b32_e32 v75, v31
	v_pk_fma_f32 v[70:71], v[70:71], v[70:71], v[72:73]
	v_mov_b32_e32 v72, v32
	v_mov_b32_e32 v73, v30
	v_pk_mul_f32 v[74:75], v[74:75], v[74:75]
	v_fmamk_f32 v29, v69, 0xba000000, v29
	v_pk_fma_f32 v[72:73], v[72:73], v[72:73], v[74:75]
	v_fmac_f32_e32 v28, 0xba000000, v69
	v_pk_add_f32 v[70:71], v[70:71], v[72:73]
	v_fmamk_f32 v27, v69, 0xba000000, v27
	v_fmac_f32_e32 v26, 0xba000000, v69
	v_pk_add_f32 v[70:71], v[70:71], v[70:71] op_sel_hi:[0,1]
	v_pk_mul_f32 v[72:73], v[26:27], v[26:27]
	v_pk_mul_f32 v[74:75], v[28:29], v[28:29]
	v_fmac_f32_e32 v40, 0xba000000, v69
	v_pk_mov_b32 v[76:77], v[74:75], v[72:73] op_sel:[1,0]
	v_mov_b32_e32 v75, v73
	v_fmamk_f32 v41, v69, 0xba000000, v41
	v_fmac_f32_e32 v38, 0xba000000, v69
	v_mul_f32_e32 v70, v40, v40
	v_pk_add_f32 v[72:73], v[76:77], v[74:75]
	v_fmamk_f32 v39, v69, 0xba000000, v39
	v_pk_fma_f32 v[74:75], v[40:41], v[40:41], v[70:71] op_sel_hi:[1,1,0]
	v_mul_f32_e32 v70, v38, v38
	v_pk_add_f32 v[72:73], v[72:73], v[72:73] op_sel_hi:[0,1]
	v_pk_fma_f32 v[76:77], v[38:39], v[38:39], v[70:71] op_sel_hi:[1,1,0]
	v_fmamk_f32 v43, v69, 0xba000000, v43
	v_fmac_f32_e32 v42, 0xba000000, v69
	v_fmamk_f32 v45, v69, 0xba000000, v45
	v_fmac_f32_e32 v44, 0xba000000, v69
	v_mul_f32_e32 v74, v44, v44
	v_mul_f32_e32 v76, v45, v45
	v_mul_f32_e32 v72, v42, v42
	v_mul_f32_e32 v70, v43, v43
	v_pk_add_f32 v[74:75], v[74:75], v[76:77]
	v_pk_add_f32 v[70:71], v[72:73], v[70:71]
	v_fmamk_f32 v49, v69, 0xba000000, v49
	v_pk_add_f32 v[70:71], v[74:75], v[70:71]
	v_fmac_f32_e32 v48, 0xba000000, v69
	v_fmamk_f32 v47, v69, 0xba000000, v47
	v_fmac_f32_e32 v46, 0xba000000, v69
	v_pk_add_f32 v[70:71], v[70:71], v[70:71] op_sel_hi:[0,1]
	v_pk_mul_f32 v[72:73], v[46:47], v[46:47]
	v_pk_mul_f32 v[74:75], v[48:49], v[48:49]
	v_fmac_f32_e32 v52, 0xba000000, v69
	v_pk_mov_b32 v[76:77], v[74:75], v[72:73] op_sel:[1,0]
	v_mov_b32_e32 v75, v73
	v_fmamk_f32 v53, v69, 0xba000000, v53
	v_fmac_f32_e32 v50, 0xba000000, v69
	v_mul_f32_e32 v70, v52, v52
	v_pk_add_f32 v[72:73], v[76:77], v[74:75]
	v_fmamk_f32 v51, v69, 0xba000000, v51
	v_pk_fma_f32 v[74:75], v[52:53], v[52:53], v[70:71] op_sel_hi:[1,1,0]
	v_mul_f32_e32 v70, v50, v50
	v_pk_add_f32 v[72:73], v[72:73], v[72:73] op_sel_hi:[0,1]
	v_pk_fma_f32 v[76:77], v[50:51], v[50:51], v[70:71] op_sel_hi:[1,1,0]
	v_fmamk_f32 v55, v69, 0xba000000, v55
	v_fmac_f32_e32 v54, 0xba000000, v69
	v_fmamk_f32 v57, v69, 0xba000000, v57
	v_fmac_f32_e32 v56, 0xba000000, v69
	v_mul_f32_e32 v74, v56, v56
	v_mul_f32_e32 v76, v57, v57
	v_mul_f32_e32 v72, v54, v54
	v_mul_f32_e32 v70, v55, v55
	v_pk_add_f32 v[74:75], v[74:75], v[76:77]
	v_pk_add_f32 v[70:71], v[72:73], v[70:71]
	s_nop 0
	v_pk_add_f32 v[70:71], v[74:75], v[70:71]
	s_nop 0
	v_add_f32_e32 v69, v70, v71
	s_nop 1
	v_mov_b32_dpp v78, v69 quad_perm:[1,0,3,2] row_mask:0xf bank_mask:0xf
	global_load_dwordx4 v[70:73], v[2:3], off
	global_load_dwordx4 v[74:77], v[4:5], off
	s_waitcnt lgkmcnt(0)
	v_add_f32_e32 v69, v69, v78
	s_nop 1
	v_mov_b32_dpp v94, v69 quad_perm:[2,3,0,1] row_mask:0xf bank_mask:0xf
	global_load_dwordx4 v[78:81], v[2:3], off offset:1024
	global_load_dwordx4 v[82:85], v[4:5], off offset:1024
	global_load_dwordx4 v[86:89], v[2:3], off offset:2048
	global_load_dwordx4 v[90:93], v[4:5], off offset:2048
	s_waitcnt lgkmcnt(0)
	v_add_f32_e32 v69, v69, v94
	s_nop 1
	v_mov_b32_dpp v110, v69 row_half_mirror row_mask:0xf bank_mask:0xf
	global_load_dwordx4 v[94:97], v[2:3], off offset:3072
	global_load_dwordx4 v[98:101], v[4:5], off offset:3072
	global_load_dwordx4 v[102:105], v[6:7], off
	global_load_dwordx4 v[106:109], v[8:9], off
	s_waitcnt lgkmcnt(0)
	v_add_f32_e32 v69, v69, v110
	s_nop 1
	v_mov_b32_dpp v126, v69 row_mirror row_mask:0xf bank_mask:0xf
	global_load_dwordx4 v[110:113], v[10:11], off
	global_load_dwordx4 v[114:117], v[12:13], off
	global_load_dwordx4 v[118:121], v[14:15], off
	global_load_dwordx4 v[122:125], v[16:17], off
	s_waitcnt lgkmcnt(0)
	v_add_f32_e32 v69, v69, v126
	global_load_dwordx4 v[126:129], v[18:19], off
	global_load_dwordx4 v[130:133], v[20:21], off
	v_mov_b32_e32 v134, v69
	s_nop 1
	v_permlane16_swap_b32_e32 v134, v69
	s_waitcnt lgkmcnt(0)
	v_add_f32_e32 v69, v69, v134
	v_mov_b32_e32 v134, v69
	s_nop 1
	v_permlane32_swap_b32_e32 v134, v69
	s_waitcnt lgkmcnt(0)
	v_add_f32_e32 v69, v69, v134
	v_fmamk_f32 v69, v69, 0x3a000000, v59
	v_mul_f32_e32 v134, 0x4f800000, v69
	v_cmp_gt_f32_e32 vcc, s21, v69
	s_nop 1
	v_cndmask_b32_e32 v69, v69, v134, vcc
	v_sqrt_f32_e32 v134, v69
	s_nop 0
	v_add_u32_e32 v135, -1, v134
	v_fma_f32 v136, -v135, v134, v69
	v_cmp_ge_f32_e64 s[0:1], 0, v136
	v_add_u32_e32 v136, 1, v134
	s_nop 0
	v_cndmask_b32_e64 v135, v134, v135, s[0:1]
	v_fma_f32 v134, -v136, v134, v69
	v_cmp_lt_f32_e64 s[0:1], 0, v134
	s_nop 1
	v_cndmask_b32_e64 v134, v135, v136, s[0:1]
	v_mul_f32_e32 v135, 0x37800000, v134
	v_cndmask_b32_e32 v134, v134, v135, vcc
	v_cmp_class_f32_e32 vcc, v69, v60
	s_nop 1
	v_cndmask_b32_e32 v69, v134, v69, vcc
	v_div_scale_f32 v134, s[0:1], v69, v69, 1.0
	v_rcp_f32_e32 v135, v134
	s_lshl_b64 s[0:1], s[4:5], 13
	s_add_u32 s0, s64, s0
	s_addc_u32 s1, s65, s1
	v_fma_f32 v136, -v134, v135, 1.0
	v_fmac_f32_e32 v135, v136, v135
	v_div_scale_f32 v136, vcc, 1.0, v69, 1.0
	v_mul_f32_e32 v137, v136, v135
	v_fma_f32 v138, -v134, v137, v136
	v_fmac_f32_e32 v137, v138, v135
	v_fma_f32 v134, -v134, v137, v136
	v_div_fmas_f32 v134, v134, v135, v137
	v_div_fixup_f32 v134, v134, v69, 1.0
	v_pk_mul_f32 v[32:33], v[32:33], v[134:135] op_sel_hi:[1,0]
	v_pk_mul_f32 v[34:35], v[34:35], v[134:135] op_sel_hi:[1,0]
	v_pk_mul_f32 v[30:31], v[30:31], v[134:135] op_sel_hi:[1,0]
	v_pk_mul_f32 v[36:37], v[36:37], v[134:135] op_sel_hi:[1,0]
	s_waitcnt vmcnt(14)
	v_pk_fma_f32 v[72:73], v[72:73], v[32:33], v[76:77]
	v_pk_mul_f32 v[26:27], v[26:27], v[134:135] op_sel_hi:[1,0]
	v_pk_fma_f32 v[70:71], v[70:71], v[36:37], v[74:75]
	s_waitcnt vmcnt(12)
	v_pk_fma_f32 v[32:33], v[80:81], v[30:31], v[84:85]
	v_pk_fma_f32 v[30:31], v[78:79], v[34:35], v[82:83]
	v_pk_mul_f32 v[34:35], v[28:29], v[134:135] op_sel_hi:[1,0]
	s_waitcnt vmcnt(10)
	v_pk_fma_f32 v[28:29], v[88:89], v[26:27], v[92:93]
	v_pk_fma_f32 v[26:27], v[86:87], v[34:35], v[90:91]
	v_pk_mul_f32 v[34:35], v[40:41], v[134:135] op_sel_hi:[1,0]
	v_pk_mul_f32 v[36:37], v[38:39], v[134:135] op_sel_hi:[1,0]
	v_pk_mul_f32 v[38:39], v[44:45], v[134:135] op_sel_hi:[1,0]
	v_pk_mul_f32 v[44:45], v[46:47], v[134:135] op_sel_hi:[1,0]
	v_pk_mul_f32 v[46:47], v[52:53], v[134:135] op_sel_hi:[1,0]
	v_pk_mul_f32 v[52:53], v[54:55], v[134:135] op_sel_hi:[1,0]
	v_lshl_add_u64 v[54:55], v[0:1], 2, s[0:1]
	s_waitcnt vmcnt(8)
	v_pk_fma_f32 v[36:37], v[96:97], v[36:37], v[100:101]
	v_pk_fma_f32 v[34:35], v[94:95], v[34:35], v[98:99]
	v_pk_mul_f32 v[40:41], v[42:43], v[134:135] op_sel_hi:[1,0]
	global_store_dwordx4 v[54:55], v[70:73], off
	global_store_dwordx4 v[54:55], v[30:33], off offset:1024
	global_store_dwordx4 v[54:55], v[26:29], off offset:2048
	global_store_dwordx4 v[54:55], v[34:37], off offset:3072
	s_waitcnt vmcnt(10)
	v_pk_fma_f32 v[40:41], v[104:105], v[40:41], v[108:109]
	v_add_co_u32_e32 v26, vcc, 0x1000, v54
	v_pk_fma_f32 v[38:39], v[102:103], v[38:39], v[106:107]
	v_pk_mul_f32 v[42:43], v[48:49], v[134:135] op_sel_hi:[1,0]
	v_pk_mul_f32 v[48:49], v[50:51], v[134:135] op_sel_hi:[1,0]
	v_pk_mul_f32 v[50:51], v[56:57], v[134:135] op_sel_hi:[1,0]
	v_addc_co_u32_e32 v27, vcc, 0, v55, vcc
	s_waitcnt vmcnt(8)
	v_pk_fma_f32 v[44:45], v[112:113], v[44:45], v[116:117]
	v_pk_fma_f32 v[42:43], v[110:111], v[42:43], v[114:115]
	s_waitcnt vmcnt(6)
	v_pk_fma_f32 v[48:49], v[120:121], v[48:49], v[124:125]
	v_pk_fma_f32 v[46:47], v[118:119], v[46:47], v[122:123]
	s_waitcnt vmcnt(4)
	v_pk_fma_f32 v[52:53], v[128:129], v[52:53], v[132:133]
	v_pk_fma_f32 v[50:51], v[126:127], v[50:51], v[130:131]
	global_store_dwordx4 v[26:27], v[38:41], off
	global_store_dwordx4 v[26:27], v[42:45], off offset:1024
	global_store_dwordx4 v[26:27], v[46:49], off offset:2048
	global_store_dwordx4 v[26:27], v[50:53], off offset:3072
	s_branch .LBB0_2072
